# residual-add epilogues (out-proj, dense FFN down): base rows prefetched with counted vmcnt; MoE leftover tiles visited panel-quarter-major for L2 reuse
# baseline (speedup 1.0000x reference)
; __device__ __forceinline__ unsigned pk2(float lo, float hi) { f32x2 v = {lo, hi}; return __builtin_bit_cast(unsigned, __builtin_convertvector(v, bf2_t)); }
; template <int BIT = 0> __device__ __forceinline__ void st16w(void* p, u32x4 v) { if ((WT_STORES >> BIT) & 1) asm volatile("global_store_dwordx4 %0, %1, off sc1\n\ts_nop 1" :: "v"(p), "v"(v) : "memory"); else *(u32x4*)p = v; }
; __device__ __forceinline__ float bflo(unsigned u) { return __uint_as_float(u << 16); }
; __device__ __forceinline__ float bfhi(unsigned u) { return __uint_as_float(u & 0xffff0000u); }
;     __device__ __forceinline__ void operator()(const f32x4 (&acc)[2][2][4][2], const Unit& u, int wr, int wc, int fr, int fq) const {
;         const int row0 = u.pm * BM + wr * 64 + fr, col0 = u.pn * BM + wc * 32 + 8 * fq;
;         const float* gv = gate + (size_t)(u.pm < 32 ? 0 : (u.pm < 64 ? 1 : 2)) * 6 * D;
;         f32x4 g4[2][2];
; #pragma unroll
;         for (int bj = 0; bj < 2; ++bj)
; #pragma unroll
;             for (int n = 0; n < 2; ++n) g4[bj][n] = *(const f32x4*)(gv + col0 + bj * HALF + 4 * n);
; #pragma unroll
;         for (int ai = 0; ai < 2; ++ai)
; #pragma unroll
;             for (int m = 0; m < 4; ++m) { const size_t ro = (size_t)(row0 + ai * HALF + m * 16) * D + col0;
; #pragma unroll
;                 for (int bj = 0; bj < 2; ++bj) { const size_t off = ro + bj * HALF;
;                     f32x4 b0, b1;
;                     if (base32) { b0 = *(const f32x4*)(base32 + off); b1 = *(const f32x4*)(base32 + off + 4); }
;                     else { const u32x4 hb = *(const u32x4*)(base + off); b0 = (f32x4){bflo(hb.x), bfhi(hb.x), bflo(hb.y), bfhi(hb.y)}; b1 = (f32x4){bflo(hb.z), bfhi(hb.z), bflo(hb.w), bfhi(hb.w)}; }
;                     const f32x4 o0 = b0 + g4[bj][0] * acc[ai][bj][m][0], o1 = b1 + g4[bj][1] * acc[ai][bj][m][1];
;                     u32x4 w; w.x = pk2(o0[0], o0[1]); w.y = pk2(o0[2], o0[3]); w.z = pk2(o1[0], o1[1]); w.w = pk2(o1[2], o1[3]);
;                     st16w(H + off, w); } }
;     }
.LBB13_929:
	s_cmp_lt_i32 s6, 64
	s_movk_i32 s7, 0x1800
	s_cselect_b32 s7, s7, 0x3000
	s_cmp_gt_i32 s6, 31
	s_cselect_b32 s7, s7, 0
	s_lshl_b32 s76, s7, 2
	v_readfirstlane_b32 s98, v168
	v_readfirstlane_b32 s99, v169
	v_lshl_or_b32 v81, s28, 8, v185
	v_lshl_add_u32 v80, s6, 8, v99
	s_nop 1
	v_readfirstlane_b32 s28, v156
	v_readfirstlane_b32 s29, v157
	v_cndmask_b32_e64 v74, 0, 1, s[18:19]
	s_nop 1
	v_cmp_ne_u32_e64 s[6:7], 1, v74
	s_movk_i32 s86, 0x1c00
	s_movk_i32 s89, 0x1600
	s_mov_b32 s88, 0x16000
	s_add_u32 s98, s98, s76
	s_addc_u32 s99, s99, 0
	v_lshlrev_b32_e32 v78, 2, v81
	global_load_dwordx4 v[90:93], v78, s[98:99] offset:16
	global_load_dwordx4 v[82:85], v78, s[98:99]
	global_load_dwordx4 v[152:155], v78, s[98:99] offset:528
	global_load_dwordx4 v[148:151], v78, s[98:99] offset:512
	v_lshlrev_b32_e32 v79, 11, v80
	v_lshl_add_u32 v79, v81, 1, v79
	v_lshlrev_b32_e32 v78, 12, v80
	v_lshl_add_u32 v78, v81, 2, v78
	s_andn2_b64 vcc, exec, s[18:19]
	s_cbranch_vccnz .Lresid_out_bf16
	global_load_dwordx4 v[174:177], v78, s[14:15]
	global_load_dwordx4 v[178:181], v78, s[14:15] offset:16
	global_load_dwordx4 v[188:191], v78, s[14:15] offset:512
	global_load_dwordx4 v[192:195], v78, s[14:15] offset:528
	v_add_u32_e32 v80, 0x10000, v78
	global_load_dwordx4 v[196:199], v80, s[14:15]
	global_load_dwordx4 v[208:211], v80, s[14:15] offset:16
	v_add_u32_e32 v80, 0x10000, v78
	global_load_dwordx4 v[212:215], v80, s[14:15] offset:512
	global_load_dwordx4 v[216:219], v80, s[14:15] offset:528
	v_add_u32_e32 v80, 0x20000, v78
	global_load_dwordx4 v[220:223], v80, s[14:15]
	global_load_dwordx4 v[224:227], v80, s[14:15] offset:16
	s_waitcnt vmcnt(8)
	v_pk_fma_f32 v[144:145], v[144:145], v[82:83], v[174:175]
	v_pk_fma_f32 v[146:147], v[146:147], v[84:85], v[176:177]
	v_pk_fma_f32 v[140:141], v[140:141], v[90:91], v[178:179]
	v_pk_fma_f32 v[142:143], v[142:143], v[92:93], v[180:181]
	v_cvt_pk_bf16_f32 v144, v144, v145
	v_cvt_pk_bf16_f32 v145, v146, v147
	v_cvt_pk_bf16_f32 v146, v140, v141
	v_cvt_pk_bf16_f32 v147, v142, v143
	global_store_dwordx4 v79, v[144:147], s[28:29]
	v_add_u32_e32 v80, 0x20000, v78
	global_load_dwordx4 v[174:177], v80, s[14:15] offset:512
	global_load_dwordx4 v[178:181], v80, s[14:15] offset:528
	s_waitcnt vmcnt(9)
	v_pk_fma_f32 v[136:137], v[136:137], v[148:149], v[188:189]
	v_pk_fma_f32 v[138:139], v[138:139], v[150:151], v[190:191]
	v_pk_fma_f32 v[132:133], v[132:133], v[152:153], v[192:193]
	v_pk_fma_f32 v[134:135], v[134:135], v[154:155], v[194:195]
	v_cvt_pk_bf16_f32 v136, v136, v137
	v_cvt_pk_bf16_f32 v137, v138, v139
	v_cvt_pk_bf16_f32 v138, v132, v133
	v_cvt_pk_bf16_f32 v139, v134, v135
	global_store_dwordx4 v79, v[136:139], s[28:29] offset:256
	v_add_u32_e32 v80, 0x30000, v78
	global_load_dwordx4 v[140:143], v80, s[14:15]
	global_load_dwordx4 v[188:191], v80, s[14:15] offset:16
	v_add_u32_e32 v80, 0x30000, v78
	global_load_dwordx4 v[192:195], v80, s[14:15] offset:512
	global_load_dwordx4 v[132:135], v80, s[14:15] offset:528
	s_waitcnt vmcnt(12)
	v_pk_fma_f32 v[128:129], v[128:129], v[82:83], v[196:197]
	v_pk_fma_f32 v[130:131], v[130:131], v[84:85], v[198:199]
	v_pk_fma_f32 v[124:125], v[124:125], v[90:91], v[208:209]
	v_pk_fma_f32 v[126:127], v[126:127], v[92:93], v[210:211]
	v_cvt_pk_bf16_f32 v128, v128, v129
	v_cvt_pk_bf16_f32 v129, v130, v131
	v_cvt_pk_bf16_f32 v130, v124, v125
	v_cvt_pk_bf16_f32 v131, v126, v127
	v_add_u32_e32 v81, 0x8000, v79
	global_store_dwordx4 v81, v[128:131], s[28:29]
	v_add_u32_e32 v80, 0x80000, v78
	global_load_dwordx4 v[196:199], v80, s[14:15]
	global_load_dwordx4 v[208:211], v80, s[14:15] offset:16
	s_waitcnt vmcnt(13)
	v_pk_fma_f32 v[120:121], v[120:121], v[148:149], v[212:213]
	v_pk_fma_f32 v[122:123], v[122:123], v[150:151], v[214:215]
	v_pk_fma_f32 v[116:117], v[116:117], v[152:153], v[216:217]
	v_pk_fma_f32 v[118:119], v[118:119], v[154:155], v[218:219]
	v_cvt_pk_bf16_f32 v120, v120, v121
	v_cvt_pk_bf16_f32 v121, v122, v123
	v_cvt_pk_bf16_f32 v122, v116, v117
	v_cvt_pk_bf16_f32 v123, v118, v119
	v_add_u32_e32 v81, 0x8000, v79
	global_store_dwordx4 v81, v[120:123], s[28:29] offset:256
	v_add_u32_e32 v80, 0x80000, v78
	global_load_dwordx4 v[124:127], v80, s[14:15] offset:512
	global_load_dwordx4 v[212:215], v80, s[14:15] offset:528
	v_add_u32_e32 v80, 0x90000, v78
	global_load_dwordx4 v[216:219], v80, s[14:15]
	global_load_dwordx4 v[116:119], v80, s[14:15] offset:16
	s_waitcnt vmcnt(16)
	v_pk_fma_f32 v[112:113], v[112:113], v[82:83], v[220:221]
	v_pk_fma_f32 v[114:115], v[114:115], v[84:85], v[222:223]
	v_pk_fma_f32 v[108:109], v[108:109], v[90:91], v[224:225]
	v_pk_fma_f32 v[110:111], v[110:111], v[92:93], v[226:227]
	v_cvt_pk_bf16_f32 v112, v112, v113
	v_cvt_pk_bf16_f32 v113, v114, v115
	v_cvt_pk_bf16_f32 v114, v108, v109
	v_cvt_pk_bf16_f32 v115, v110, v111
	v_add_u32_e32 v81, 0x10000, v79
	global_store_dwordx4 v81, v[112:115], s[28:29]
	v_add_u32_e32 v80, 0x90000, v78
	global_load_dwordx4 v[220:223], v80, s[14:15] offset:512
	global_load_dwordx4 v[224:227], v80, s[14:15] offset:528
	s_waitcnt vmcnt(16)
	v_pk_fma_f32 v[104:105], v[104:105], v[148:149], v[174:175]
	v_pk_fma_f32 v[106:107], v[106:107], v[150:151], v[176:177]
	v_pk_fma_f32 v[100:101], v[100:101], v[152:153], v[178:179]
	v_pk_fma_f32 v[102:103], v[102:103], v[154:155], v[180:181]
	v_cvt_pk_bf16_f32 v104, v104, v105
	v_cvt_pk_bf16_f32 v105, v106, v107
	v_cvt_pk_bf16_f32 v106, v100, v101
	v_cvt_pk_bf16_f32 v107, v102, v103
	v_add_u32_e32 v81, 0x10000, v79
	global_store_dwordx4 v81, v[104:107], s[28:29] offset:256
	v_add_u32_e32 v80, 0xa0000, v78
	global_load_dwordx4 v[108:111], v80, s[14:15]
	global_load_dwordx4 v[174:177], v80, s[14:15] offset:16
	v_add_u32_e32 v80, 0xa0000, v78
	global_load_dwordx4 v[178:181], v80, s[14:15] offset:512
	global_load_dwordx4 v[100:103], v80, s[14:15] offset:528
	s_waitcnt vmcnt(18)
; __device__ __forceinline__ unsigned pk2(float lo, float hi) { f32x2 v = {lo, hi}; return __builtin_bit_cast(unsigned, __builtin_convertvector(v, bf2_t)); }
; template <int BIT = 0> __device__ __forceinline__ void st16w(void* p, u32x4 v) { if ((WT_STORES >> BIT) & 1) asm volatile("global_store_dwordx4 %0, %1, off sc1\n\ts_nop 1" :: "v"(p), "v"(v) : "memory"); else *(u32x4*)p = v; }
; __device__ __forceinline__ float bflo(unsigned u) { return __uint_as_float(u << 16); }
; __device__ __forceinline__ float bfhi(unsigned u) { return __uint_as_float(u & 0xffff0000u); }
;     __device__ __forceinline__ void operator()(const f32x4 (&acc)[2][2][4][2], const Unit& u, int wr, int wc, int fr, int fq) const {
;     ...
;         for (int ai = 0; ai < 2; ++ai)
; #pragma unroll
;             for (int m = 0; m < 4; ++m) { const size_t ro = (size_t)(row0 + ai * HALF + m * 16) * D + col0;
; #pragma unroll
;                 for (int bj = 0; bj < 2; ++bj) { const size_t off = ro + bj * HALF;
;                     f32x4 b0, b1;
;                     if (base32) { b0 = *(const f32x4*)(base32 + off); b1 = *(const f32x4*)(base32 + off + 4); }
;                     else { const u32x4 hb = *(const u32x4*)(base + off); b0 = (f32x4){bflo(hb.x), bfhi(hb.x), bflo(hb.y), bfhi(hb.y)}; b1 = (f32x4){bflo(hb.z), bfhi(hb.z), bflo(hb.w), bfhi(hb.w)}; }
;                     const f32x4 o0 = b0 + g4[bj][0] * acc[ai][bj][m][0], o1 = b1 + g4[bj][1] * acc[ai][bj][m][1];
;                     u32x4 w; w.x = pk2(o0[0], o0[1]); w.y = pk2(o0[2], o0[3]); w.z = pk2(o1[0], o1[1]); w.w = pk2(o1[2], o1[3]);
;                     st16w(H + off, w); } }
	v_pk_fma_f32 v[94:95], v[94:95], v[82:83], v[140:141]
	v_pk_fma_f32 v[96:97], v[96:97], v[84:85], v[142:143]
	v_pk_fma_f32 v[86:87], v[86:87], v[90:91], v[188:189]
	v_pk_fma_f32 v[88:89], v[88:89], v[92:93], v[190:191]
	v_cvt_pk_bf16_f32 v94, v94, v95
	v_cvt_pk_bf16_f32 v95, v96, v97
	v_cvt_pk_bf16_f32 v96, v86, v87
	v_cvt_pk_bf16_f32 v97, v88, v89
	v_add_u32_e32 v81, 0x18000, v79
	global_store_dwordx4 v81, v[94:97], s[28:29]
	v_add_u32_e32 v80, 0xb0000, v78
	global_load_dwordx4 v[140:143], v80, s[14:15]
	global_load_dwordx4 v[188:191], v80, s[14:15] offset:16
	s_waitcnt vmcnt(19)
	v_pk_fma_f32 v[70:71], v[70:71], v[148:149], v[192:193]
	v_pk_fma_f32 v[72:73], v[72:73], v[150:151], v[194:195]
	v_pk_fma_f32 v[66:67], v[66:67], v[152:153], v[132:133]
	v_pk_fma_f32 v[68:69], v[68:69], v[154:155], v[134:135]
	v_cvt_pk_bf16_f32 v70, v70, v71
	v_cvt_pk_bf16_f32 v71, v72, v73
	v_cvt_pk_bf16_f32 v72, v66, v67
	v_cvt_pk_bf16_f32 v73, v68, v69
	v_add_u32_e32 v81, 0x18000, v79
	global_store_dwordx4 v81, v[70:73], s[28:29] offset:256
	v_add_u32_e32 v80, 0xb0000, v78
	global_load_dwordx4 v[86:89], v80, s[14:15] offset:512
	global_load_dwordx4 v[192:195], v80, s[14:15] offset:528
	s_waitcnt vmcnt(19)
	v_pk_fma_f32 v[62:63], v[62:63], v[82:83], v[196:197]
	v_pk_fma_f32 v[64:65], v[64:65], v[84:85], v[198:199]
	v_pk_fma_f32 v[58:59], v[58:59], v[90:91], v[208:209]
	v_pk_fma_f32 v[60:61], v[60:61], v[92:93], v[210:211]
	v_cvt_pk_bf16_f32 v62, v62, v63
	v_cvt_pk_bf16_f32 v63, v64, v65
	v_cvt_pk_bf16_f32 v64, v58, v59
	v_cvt_pk_bf16_f32 v65, v60, v61
	v_add_u32_e32 v81, 0x40000, v79
	global_store_dwordx4 v81, v[62:65], s[28:29]
	s_waitcnt vmcnt(17)
	v_pk_fma_f32 v[54:55], v[54:55], v[148:149], v[124:125]
	v_pk_fma_f32 v[56:57], v[56:57], v[150:151], v[126:127]
	v_pk_fma_f32 v[50:51], v[50:51], v[152:153], v[212:213]
	v_pk_fma_f32 v[52:53], v[52:53], v[154:155], v[214:215]
	v_cvt_pk_bf16_f32 v54, v54, v55
	v_cvt_pk_bf16_f32 v55, v56, v57
	v_cvt_pk_bf16_f32 v56, v50, v51
	v_cvt_pk_bf16_f32 v57, v52, v53
	v_add_u32_e32 v81, 0x40000, v79
	global_store_dwordx4 v81, v[54:57], s[28:29] offset:256
	s_waitcnt vmcnt(16)
	v_pk_fma_f32 v[46:47], v[46:47], v[82:83], v[216:217]
	v_pk_fma_f32 v[48:49], v[48:49], v[84:85], v[218:219]
	v_pk_fma_f32 v[42:43], v[42:43], v[90:91], v[116:117]
	v_pk_fma_f32 v[44:45], v[44:45], v[92:93], v[118:119]
	v_cvt_pk_bf16_f32 v46, v46, v47
	v_cvt_pk_bf16_f32 v47, v48, v49
	v_cvt_pk_bf16_f32 v48, v42, v43
	v_cvt_pk_bf16_f32 v49, v44, v45
	v_add_u32_e32 v81, 0x48000, v79
	global_store_dwordx4 v81, v[46:49], s[28:29]
	s_waitcnt vmcnt(14)
	v_pk_fma_f32 v[38:39], v[38:39], v[148:149], v[220:221]
	v_pk_fma_f32 v[40:41], v[40:41], v[150:151], v[222:223]
	v_pk_fma_f32 v[34:35], v[34:35], v[152:153], v[224:225]
	v_pk_fma_f32 v[36:37], v[36:37], v[154:155], v[226:227]
	v_cvt_pk_bf16_f32 v38, v38, v39
	v_cvt_pk_bf16_f32 v39, v40, v41
	v_cvt_pk_bf16_f32 v40, v34, v35
	v_cvt_pk_bf16_f32 v41, v36, v37
	v_add_u32_e32 v81, 0x48000, v79
	global_store_dwordx4 v81, v[38:41], s[28:29] offset:256
	s_waitcnt vmcnt(12)
	v_pk_fma_f32 v[30:31], v[30:31], v[82:83], v[108:109]
	v_pk_fma_f32 v[32:33], v[32:33], v[84:85], v[110:111]
	v_pk_fma_f32 v[26:27], v[26:27], v[90:91], v[174:175]
	v_pk_fma_f32 v[28:29], v[28:29], v[92:93], v[176:177]
	v_cvt_pk_bf16_f32 v30, v30, v31
	v_cvt_pk_bf16_f32 v31, v32, v33
	v_cvt_pk_bf16_f32 v32, v26, v27
	v_cvt_pk_bf16_f32 v33, v28, v29
	v_add_u32_e32 v81, 0x50000, v79
	global_store_dwordx4 v81, v[30:33], s[28:29]
	s_waitcnt vmcnt(11)
	v_pk_fma_f32 v[22:23], v[22:23], v[148:149], v[178:179]
	v_pk_fma_f32 v[24:25], v[24:25], v[150:151], v[180:181]
	v_pk_fma_f32 v[18:19], v[18:19], v[152:153], v[100:101]
	v_pk_fma_f32 v[20:21], v[20:21], v[154:155], v[102:103]
	v_cvt_pk_bf16_f32 v22, v22, v23
	v_cvt_pk_bf16_f32 v23, v24, v25
	v_cvt_pk_bf16_f32 v24, v18, v19
	v_cvt_pk_bf16_f32 v25, v20, v21
	v_add_u32_e32 v81, 0x50000, v79
	global_store_dwordx4 v81, v[22:25], s[28:29] offset:256
	s_waitcnt vmcnt(9)
	v_pk_fma_f32 v[14:15], v[14:15], v[82:83], v[140:141]
	v_pk_fma_f32 v[16:17], v[16:17], v[84:85], v[142:143]
	v_pk_fma_f32 v[10:11], v[10:11], v[90:91], v[188:189]
	v_pk_fma_f32 v[12:13], v[12:13], v[92:93], v[190:191]
	v_cvt_pk_bf16_f32 v14, v14, v15
	v_cvt_pk_bf16_f32 v15, v16, v17
	v_cvt_pk_bf16_f32 v16, v10, v11
	v_cvt_pk_bf16_f32 v17, v12, v13
	v_add_u32_e32 v81, 0x58000, v79
	global_store_dwordx4 v81, v[14:17], s[28:29]
	s_waitcnt vmcnt(7)
	v_pk_fma_f32 v[6:7], v[6:7], v[148:149], v[86:87]
	v_pk_fma_f32 v[8:9], v[8:9], v[150:151], v[88:89]
	v_pk_fma_f32 v[2:3], v[2:3], v[152:153], v[192:193]
	v_pk_fma_f32 v[4:5], v[4:5], v[154:155], v[194:195]
	v_cvt_pk_bf16_f32 v6, v6, v7
	v_cvt_pk_bf16_f32 v7, v8, v9
	v_cvt_pk_bf16_f32 v8, v2, v3
	v_cvt_pk_bf16_f32 v9, v4, v5
	v_add_u32_e32 v81, 0x58000, v79
	global_store_dwordx4 v81, v[6:9], s[28:29] offset:256
	s_nop 1
	s_branch .Lresid_out_done
; __device__ __forceinline__ unsigned pk2(float lo, float hi) { f32x2 v = {lo, hi}; return __builtin_bit_cast(unsigned, __builtin_convertvector(v, bf2_t)); }
; template <int BIT = 0> __device__ __forceinline__ void st16w(void* p, u32x4 v) { if ((WT_STORES >> BIT) & 1) asm volatile("global_store_dwordx4 %0, %1, off sc1\n\ts_nop 1" :: "v"(p), "v"(v) : "memory"); else *(u32x4*)p = v; }
; __device__ __forceinline__ float bflo(unsigned u) { return __uint_as_float(u << 16); }
; __device__ __forceinline__ float bfhi(unsigned u) { return __uint_as_float(u & 0xffff0000u); }
;     __device__ __forceinline__ void operator()(const f32x4 (&acc)[2][2][4][2], const Unit& u, int wr, int wc, int fr, int fq) const {
;     ...
;         for (int ai = 0; ai < 2; ++ai)
; #pragma unroll
;             for (int m = 0; m < 4; ++m) { const size_t ro = (size_t)(row0 + ai * HALF + m * 16) * D + col0;
; #pragma unroll
;                 for (int bj = 0; bj < 2; ++bj) { const size_t off = ro + bj * HALF;
;                     f32x4 b0, b1;
;                     if (base32) { b0 = *(const f32x4*)(base32 + off); b1 = *(const f32x4*)(base32 + off + 4); }
;                     else { const u32x4 hb = *(const u32x4*)(base + off); b0 = (f32x4){bflo(hb.x), bfhi(hb.x), bflo(hb.y), bfhi(hb.y)}; b1 = (f32x4){bflo(hb.z), bfhi(hb.z), bflo(hb.w), bfhi(hb.w)}; }
;                     const f32x4 o0 = b0 + g4[bj][0] * acc[ai][bj][m][0], o1 = b1 + g4[bj][1] * acc[ai][bj][m][1];
;                     u32x4 w; w.x = pk2(o0[0], o0[1]); w.y = pk2(o0[2], o0[3]); w.z = pk2(o1[0], o1[1]); w.w = pk2(o1[2], o1[3]);
;                     st16w(H + off, w); } }
.Lresid_out_bf16:
	global_load_dwordx4 v[174:177], v79, s[28:29]
	global_load_dwordx4 v[178:181], v79, s[28:29] offset:256
	v_add_u32_e32 v80, 0x8000, v79
	global_load_dwordx4 v[188:191], v80, s[28:29]
	v_add_u32_e32 v80, 0x8000, v79
	global_load_dwordx4 v[192:195], v80, s[28:29] offset:256
	v_add_u32_e32 v80, 0x10000, v79
	global_load_dwordx4 v[196:199], v80, s[28:29]
	v_add_u32_e32 v80, 0x10000, v79
	global_load_dwordx4 v[208:211], v80, s[28:29] offset:256
	v_add_u32_e32 v80, 0x18000, v79
	global_load_dwordx4 v[212:215], v80, s[28:29]
	v_add_u32_e32 v80, 0x18000, v79
	global_load_dwordx4 v[216:219], v80, s[28:29] offset:256
	v_add_u32_e32 v80, 0x40000, v79
	global_load_dwordx4 v[220:223], v80, s[28:29]
	v_add_u32_e32 v80, 0x40000, v79
	global_load_dwordx4 v[224:227], v80, s[28:29] offset:256
	s_waitcnt vmcnt(9)
	v_lshlrev_b32_e32 v74, 16, v174
	v_and_b32_e32 v75, 0xffff0000, v174
	v_pk_fma_f32 v[144:145], v[144:145], v[82:83], v[74:75]
	v_lshlrev_b32_e32 v76, 16, v175
	v_and_b32_e32 v77, 0xffff0000, v175
	v_pk_fma_f32 v[146:147], v[146:147], v[84:85], v[76:77]
	v_lshlrev_b32_e32 v74, 16, v176
	v_and_b32_e32 v75, 0xffff0000, v176
	v_pk_fma_f32 v[140:141], v[140:141], v[90:91], v[74:75]
	v_lshlrev_b32_e32 v76, 16, v177
	v_and_b32_e32 v77, 0xffff0000, v177
	v_pk_fma_f32 v[142:143], v[142:143], v[92:93], v[76:77]
	v_cvt_pk_bf16_f32 v144, v144, v145
	v_cvt_pk_bf16_f32 v145, v146, v147
	v_cvt_pk_bf16_f32 v146, v140, v141
	v_cvt_pk_bf16_f32 v147, v142, v143
	global_store_dwordx4 v79, v[144:147], s[28:29]
	v_add_u32_e32 v80, 0x48000, v79
	global_load_dwordx4 v[174:177], v80, s[28:29]
	v_add_u32_e32 v80, 0x48000, v79
	global_load_dwordx4 v[140:143], v80, s[28:29] offset:256
	s_waitcnt vmcnt(11)
	v_lshlrev_b32_e32 v74, 16, v178
	v_and_b32_e32 v75, 0xffff0000, v178
	v_pk_fma_f32 v[136:137], v[136:137], v[148:149], v[74:75]
	v_lshlrev_b32_e32 v76, 16, v179
	v_and_b32_e32 v77, 0xffff0000, v179
	v_pk_fma_f32 v[138:139], v[138:139], v[150:151], v[76:77]
	v_lshlrev_b32_e32 v74, 16, v180
	v_and_b32_e32 v75, 0xffff0000, v180
	v_pk_fma_f32 v[132:133], v[132:133], v[152:153], v[74:75]
	v_lshlrev_b32_e32 v76, 16, v181
	v_and_b32_e32 v77, 0xffff0000, v181
	v_pk_fma_f32 v[134:135], v[134:135], v[154:155], v[76:77]
	v_cvt_pk_bf16_f32 v136, v136, v137
	v_cvt_pk_bf16_f32 v137, v138, v139
	v_cvt_pk_bf16_f32 v138, v132, v133
	v_cvt_pk_bf16_f32 v139, v134, v135
	global_store_dwordx4 v79, v[136:139], s[28:29] offset:256
	v_add_u32_e32 v80, 0x50000, v79
	global_load_dwordx4 v[178:181], v80, s[28:29]
	v_add_u32_e32 v80, 0x50000, v79
	global_load_dwordx4 v[132:135], v80, s[28:29] offset:256
	s_waitcnt vmcnt(13)
	v_lshlrev_b32_e32 v74, 16, v188
	v_and_b32_e32 v75, 0xffff0000, v188
	v_pk_fma_f32 v[128:129], v[128:129], v[82:83], v[74:75]
	v_lshlrev_b32_e32 v76, 16, v189
	v_and_b32_e32 v77, 0xffff0000, v189
	v_pk_fma_f32 v[130:131], v[130:131], v[84:85], v[76:77]
	v_lshlrev_b32_e32 v74, 16, v190
	v_and_b32_e32 v75, 0xffff0000, v190
	v_pk_fma_f32 v[124:125], v[124:125], v[90:91], v[74:75]
	v_lshlrev_b32_e32 v76, 16, v191
	v_and_b32_e32 v77, 0xffff0000, v191
	v_pk_fma_f32 v[126:127], v[126:127], v[92:93], v[76:77]
	v_cvt_pk_bf16_f32 v128, v128, v129
	v_cvt_pk_bf16_f32 v129, v130, v131
	v_cvt_pk_bf16_f32 v130, v124, v125
	v_cvt_pk_bf16_f32 v131, v126, v127
	v_add_u32_e32 v81, 0x8000, v79
	global_store_dwordx4 v81, v[128:131], s[28:29]
	v_add_u32_e32 v80, 0x58000, v79
	global_load_dwordx4 v[188:191], v80, s[28:29]
	v_add_u32_e32 v80, 0x58000, v79
	global_load_dwordx4 v[124:127], v80, s[28:29] offset:256
	s_waitcnt vmcnt(15)
	v_lshlrev_b32_e32 v74, 16, v192
	v_and_b32_e32 v75, 0xffff0000, v192
	v_pk_fma_f32 v[120:121], v[120:121], v[148:149], v[74:75]
	v_lshlrev_b32_e32 v76, 16, v193
	v_and_b32_e32 v77, 0xffff0000, v193
	v_pk_fma_f32 v[122:123], v[122:123], v[150:151], v[76:77]
	v_lshlrev_b32_e32 v74, 16, v194
	v_and_b32_e32 v75, 0xffff0000, v194
	v_pk_fma_f32 v[116:117], v[116:117], v[152:153], v[74:75]
	v_lshlrev_b32_e32 v76, 16, v195
	v_and_b32_e32 v77, 0xffff0000, v195
	v_pk_fma_f32 v[118:119], v[118:119], v[154:155], v[76:77]
	v_cvt_pk_bf16_f32 v120, v120, v121
	v_cvt_pk_bf16_f32 v121, v122, v123
	v_cvt_pk_bf16_f32 v122, v116, v117
	v_cvt_pk_bf16_f32 v123, v118, v119
	v_add_u32_e32 v81, 0x8000, v79
	global_store_dwordx4 v81, v[120:123], s[28:29] offset:256
	s_waitcnt vmcnt(15)
	v_lshlrev_b32_e32 v74, 16, v196
	v_and_b32_e32 v75, 0xffff0000, v196
	v_pk_fma_f32 v[112:113], v[112:113], v[82:83], v[74:75]
	v_lshlrev_b32_e32 v76, 16, v197
	v_and_b32_e32 v77, 0xffff0000, v197
	v_pk_fma_f32 v[114:115], v[114:115], v[84:85], v[76:77]
	v_lshlrev_b32_e32 v74, 16, v198
	v_and_b32_e32 v75, 0xffff0000, v198
	v_pk_fma_f32 v[108:109], v[108:109], v[90:91], v[74:75]
	v_lshlrev_b32_e32 v76, 16, v199
	v_and_b32_e32 v77, 0xffff0000, v199
	v_pk_fma_f32 v[110:111], v[110:111], v[92:93], v[76:77]
	v_cvt_pk_bf16_f32 v112, v112, v113
	v_cvt_pk_bf16_f32 v113, v114, v115
	v_cvt_pk_bf16_f32 v114, v108, v109
	v_cvt_pk_bf16_f32 v115, v110, v111
	v_add_u32_e32 v81, 0x10000, v79
	global_store_dwordx4 v81, v[112:115], s[28:29]
	s_waitcnt vmcnt(15)
	v_lshlrev_b32_e32 v74, 16, v208
	v_and_b32_e32 v75, 0xffff0000, v208
	v_pk_fma_f32 v[104:105], v[104:105], v[148:149], v[74:75]
	v_lshlrev_b32_e32 v76, 16, v209
	v_and_b32_e32 v77, 0xffff0000, v209
	v_pk_fma_f32 v[106:107], v[106:107], v[150:151], v[76:77]
	v_lshlrev_b32_e32 v74, 16, v210
	v_and_b32_e32 v75, 0xffff0000, v210
	v_pk_fma_f32 v[100:101], v[100:101], v[152:153], v[74:75]
	v_lshlrev_b32_e32 v76, 16, v211
	v_and_b32_e32 v77, 0xffff0000, v211
	v_pk_fma_f32 v[102:103], v[102:103], v[154:155], v[76:77]
	v_cvt_pk_bf16_f32 v104, v104, v105
	v_cvt_pk_bf16_f32 v105, v106, v107
	v_cvt_pk_bf16_f32 v106, v100, v101
	v_cvt_pk_bf16_f32 v107, v102, v103
	v_add_u32_e32 v81, 0x10000, v79
	global_store_dwordx4 v81, v[104:107], s[28:29] offset:256
	s_waitcnt vmcnt(15)
; __device__ __forceinline__ unsigned pk2(float lo, float hi) { f32x2 v = {lo, hi}; return __builtin_bit_cast(unsigned, __builtin_convertvector(v, bf2_t)); }
; template <int BIT = 0> __device__ __forceinline__ void st16w(void* p, u32x4 v) { if ((WT_STORES >> BIT) & 1) asm volatile("global_store_dwordx4 %0, %1, off sc1\n\ts_nop 1" :: "v"(p), "v"(v) : "memory"); else *(u32x4*)p = v; }
; __device__ __forceinline__ float bflo(unsigned u) { return __uint_as_float(u << 16); }
; __device__ __forceinline__ float bfhi(unsigned u) { return __uint_as_float(u & 0xffff0000u); }
;     __device__ __forceinline__ void operator()(const f32x4 (&acc)[2][2][4][2], const Unit& u, int wr, int wc, int fr, int fq) const {
;     ...
;         for (int ai = 0; ai < 2; ++ai)
; #pragma unroll
;             for (int m = 0; m < 4; ++m) { const size_t ro = (size_t)(row0 + ai * HALF + m * 16) * D + col0;
; #pragma unroll
;                 for (int bj = 0; bj < 2; ++bj) { const size_t off = ro + bj * HALF;
;                     f32x4 b0, b1;
;                     if (base32) { b0 = *(const f32x4*)(base32 + off); b1 = *(const f32x4*)(base32 + off + 4); }
;                     else { const u32x4 hb = *(const u32x4*)(base + off); b0 = (f32x4){bflo(hb.x), bfhi(hb.x), bflo(hb.y), bfhi(hb.y)}; b1 = (f32x4){bflo(hb.z), bfhi(hb.z), bflo(hb.w), bfhi(hb.w)}; }
;                     const f32x4 o0 = b0 + g4[bj][0] * acc[ai][bj][m][0], o1 = b1 + g4[bj][1] * acc[ai][bj][m][1];
;                     u32x4 w; w.x = pk2(o0[0], o0[1]); w.y = pk2(o0[2], o0[3]); w.z = pk2(o1[0], o1[1]); w.w = pk2(o1[2], o1[3]);
;                     st16w(H + off, w); } }
	v_lshlrev_b32_e32 v74, 16, v212
	v_and_b32_e32 v75, 0xffff0000, v212
	v_pk_fma_f32 v[94:95], v[94:95], v[82:83], v[74:75]
	v_lshlrev_b32_e32 v76, 16, v213
	v_and_b32_e32 v77, 0xffff0000, v213
	v_pk_fma_f32 v[96:97], v[96:97], v[84:85], v[76:77]
	v_lshlrev_b32_e32 v74, 16, v214
	v_and_b32_e32 v75, 0xffff0000, v214
	v_pk_fma_f32 v[86:87], v[86:87], v[90:91], v[74:75]
	v_lshlrev_b32_e32 v76, 16, v215
	v_and_b32_e32 v77, 0xffff0000, v215
	v_pk_fma_f32 v[88:89], v[88:89], v[92:93], v[76:77]
	v_cvt_pk_bf16_f32 v94, v94, v95
	v_cvt_pk_bf16_f32 v95, v96, v97
	v_cvt_pk_bf16_f32 v96, v86, v87
	v_cvt_pk_bf16_f32 v97, v88, v89
	v_add_u32_e32 v81, 0x18000, v79
	global_store_dwordx4 v81, v[94:97], s[28:29]
	s_waitcnt vmcnt(15)
	v_lshlrev_b32_e32 v74, 16, v216
	v_and_b32_e32 v75, 0xffff0000, v216
	v_pk_fma_f32 v[70:71], v[70:71], v[148:149], v[74:75]
	v_lshlrev_b32_e32 v76, 16, v217
	v_and_b32_e32 v77, 0xffff0000, v217
	v_pk_fma_f32 v[72:73], v[72:73], v[150:151], v[76:77]
	v_lshlrev_b32_e32 v74, 16, v218
	v_and_b32_e32 v75, 0xffff0000, v218
	v_pk_fma_f32 v[66:67], v[66:67], v[152:153], v[74:75]
	v_lshlrev_b32_e32 v76, 16, v219
	v_and_b32_e32 v77, 0xffff0000, v219
	v_pk_fma_f32 v[68:69], v[68:69], v[154:155], v[76:77]
	v_cvt_pk_bf16_f32 v70, v70, v71
	v_cvt_pk_bf16_f32 v71, v72, v73
	v_cvt_pk_bf16_f32 v72, v66, v67
	v_cvt_pk_bf16_f32 v73, v68, v69
	v_add_u32_e32 v81, 0x18000, v79
	global_store_dwordx4 v81, v[70:73], s[28:29] offset:256
	s_waitcnt vmcnt(15)
	v_lshlrev_b32_e32 v74, 16, v220
	v_and_b32_e32 v75, 0xffff0000, v220
	v_pk_fma_f32 v[62:63], v[62:63], v[82:83], v[74:75]
	v_lshlrev_b32_e32 v76, 16, v221
	v_and_b32_e32 v77, 0xffff0000, v221
	v_pk_fma_f32 v[64:65], v[64:65], v[84:85], v[76:77]
	v_lshlrev_b32_e32 v74, 16, v222
	v_and_b32_e32 v75, 0xffff0000, v222
	v_pk_fma_f32 v[58:59], v[58:59], v[90:91], v[74:75]
	v_lshlrev_b32_e32 v76, 16, v223
	v_and_b32_e32 v77, 0xffff0000, v223
	v_pk_fma_f32 v[60:61], v[60:61], v[92:93], v[76:77]
	v_cvt_pk_bf16_f32 v62, v62, v63
	v_cvt_pk_bf16_f32 v63, v64, v65
	v_cvt_pk_bf16_f32 v64, v58, v59
	v_cvt_pk_bf16_f32 v65, v60, v61
	v_add_u32_e32 v81, 0x40000, v79
	global_store_dwordx4 v81, v[62:65], s[28:29]
	s_waitcnt vmcnt(15)
	v_lshlrev_b32_e32 v74, 16, v224
	v_and_b32_e32 v75, 0xffff0000, v224
	v_pk_fma_f32 v[54:55], v[54:55], v[148:149], v[74:75]
	v_lshlrev_b32_e32 v76, 16, v225
	v_and_b32_e32 v77, 0xffff0000, v225
	v_pk_fma_f32 v[56:57], v[56:57], v[150:151], v[76:77]
	v_lshlrev_b32_e32 v74, 16, v226
	v_and_b32_e32 v75, 0xffff0000, v226
	v_pk_fma_f32 v[50:51], v[50:51], v[152:153], v[74:75]
	v_lshlrev_b32_e32 v76, 16, v227
	v_and_b32_e32 v77, 0xffff0000, v227
	v_pk_fma_f32 v[52:53], v[52:53], v[154:155], v[76:77]
	v_cvt_pk_bf16_f32 v54, v54, v55
	v_cvt_pk_bf16_f32 v55, v56, v57
	v_cvt_pk_bf16_f32 v56, v50, v51
	v_cvt_pk_bf16_f32 v57, v52, v53
	v_add_u32_e32 v81, 0x40000, v79
	global_store_dwordx4 v81, v[54:57], s[28:29] offset:256
	s_waitcnt vmcnt(14)
	v_lshlrev_b32_e32 v74, 16, v174
	v_and_b32_e32 v75, 0xffff0000, v174
	v_pk_fma_f32 v[46:47], v[46:47], v[82:83], v[74:75]
	v_lshlrev_b32_e32 v76, 16, v175
	v_and_b32_e32 v77, 0xffff0000, v175
	v_pk_fma_f32 v[48:49], v[48:49], v[84:85], v[76:77]
	v_lshlrev_b32_e32 v74, 16, v176
	v_and_b32_e32 v75, 0xffff0000, v176
	v_pk_fma_f32 v[42:43], v[42:43], v[90:91], v[74:75]
	v_lshlrev_b32_e32 v76, 16, v177
	v_and_b32_e32 v77, 0xffff0000, v177
	v_pk_fma_f32 v[44:45], v[44:45], v[92:93], v[76:77]
	v_cvt_pk_bf16_f32 v46, v46, v47
	v_cvt_pk_bf16_f32 v47, v48, v49
	v_cvt_pk_bf16_f32 v48, v42, v43
	v_cvt_pk_bf16_f32 v49, v44, v45
	v_add_u32_e32 v81, 0x48000, v79
	global_store_dwordx4 v81, v[46:49], s[28:29]
	s_waitcnt vmcnt(14)
; __device__ __forceinline__ unsigned pk2(float lo, float hi) { f32x2 v = {lo, hi}; return __builtin_bit_cast(unsigned, __builtin_convertvector(v, bf2_t)); }
; template <int BIT = 0> __device__ __forceinline__ void st16w(void* p, u32x4 v) { if ((WT_STORES >> BIT) & 1) asm volatile("global_store_dwordx4 %0, %1, off sc1\n\ts_nop 1" :: "v"(p), "v"(v) : "memory"); else *(u32x4*)p = v; }
; __device__ __forceinline__ float bflo(unsigned u) { return __uint_as_float(u << 16); }
; __device__ __forceinline__ float bfhi(unsigned u) { return __uint_as_float(u & 0xffff0000u); }
;     __device__ __forceinline__ void operator()(const f32x4 (&acc)[2][2][4][2], const Unit& u, int wr, int wc, int fr, int fq) const {
;     ...
;         for (int ai = 0; ai < 2; ++ai)
; #pragma unroll
;             for (int m = 0; m < 4; ++m) { const size_t ro = (size_t)(row0 + ai * HALF + m * 16) * D + col0;
; #pragma unroll
;                 for (int bj = 0; bj < 2; ++bj) { const size_t off = ro + bj * HALF;
;                     f32x4 b0, b1;
;                     if (base32) { b0 = *(const f32x4*)(base32 + off); b1 = *(const f32x4*)(base32 + off + 4); }
;                     else { const u32x4 hb = *(const u32x4*)(base + off); b0 = (f32x4){bflo(hb.x), bfhi(hb.x), bflo(hb.y), bfhi(hb.y)}; b1 = (f32x4){bflo(hb.z), bfhi(hb.z), bflo(hb.w), bfhi(hb.w)}; }
;                     const f32x4 o0 = b0 + g4[bj][0] * acc[ai][bj][m][0], o1 = b1 + g4[bj][1] * acc[ai][bj][m][1];
;                     u32x4 w; w.x = pk2(o0[0], o0[1]); w.y = pk2(o0[2], o0[3]); w.z = pk2(o1[0], o1[1]); w.w = pk2(o1[2], o1[3]);
;                     st16w(H + off, w); } }
	v_lshlrev_b32_e32 v74, 16, v140
	v_and_b32_e32 v75, 0xffff0000, v140
	v_pk_fma_f32 v[38:39], v[38:39], v[148:149], v[74:75]
	v_lshlrev_b32_e32 v76, 16, v141
	v_and_b32_e32 v77, 0xffff0000, v141
	v_pk_fma_f32 v[40:41], v[40:41], v[150:151], v[76:77]
	v_lshlrev_b32_e32 v74, 16, v142
	v_and_b32_e32 v75, 0xffff0000, v142
	v_pk_fma_f32 v[34:35], v[34:35], v[152:153], v[74:75]
	v_lshlrev_b32_e32 v76, 16, v143
	v_and_b32_e32 v77, 0xffff0000, v143
	v_pk_fma_f32 v[36:37], v[36:37], v[154:155], v[76:77]
	v_cvt_pk_bf16_f32 v38, v38, v39
	v_cvt_pk_bf16_f32 v39, v40, v41
	v_cvt_pk_bf16_f32 v40, v34, v35
	v_cvt_pk_bf16_f32 v41, v36, v37
	v_add_u32_e32 v81, 0x48000, v79
	global_store_dwordx4 v81, v[38:41], s[28:29] offset:256
	s_waitcnt vmcnt(13)
	v_lshlrev_b32_e32 v74, 16, v178
	v_and_b32_e32 v75, 0xffff0000, v178
	v_pk_fma_f32 v[30:31], v[30:31], v[82:83], v[74:75]
	v_lshlrev_b32_e32 v76, 16, v179
	v_and_b32_e32 v77, 0xffff0000, v179
	v_pk_fma_f32 v[32:33], v[32:33], v[84:85], v[76:77]
	v_lshlrev_b32_e32 v74, 16, v180
	v_and_b32_e32 v75, 0xffff0000, v180
	v_pk_fma_f32 v[26:27], v[26:27], v[90:91], v[74:75]
	v_lshlrev_b32_e32 v76, 16, v181
	v_and_b32_e32 v77, 0xffff0000, v181
	v_pk_fma_f32 v[28:29], v[28:29], v[92:93], v[76:77]
	v_cvt_pk_bf16_f32 v30, v30, v31
	v_cvt_pk_bf16_f32 v31, v32, v33
	v_cvt_pk_bf16_f32 v32, v26, v27
	v_cvt_pk_bf16_f32 v33, v28, v29
	v_add_u32_e32 v81, 0x50000, v79
	global_store_dwordx4 v81, v[30:33], s[28:29]
	s_waitcnt vmcnt(13)
	v_lshlrev_b32_e32 v74, 16, v132
	v_and_b32_e32 v75, 0xffff0000, v132
	v_pk_fma_f32 v[22:23], v[22:23], v[148:149], v[74:75]
	v_lshlrev_b32_e32 v76, 16, v133
	v_and_b32_e32 v77, 0xffff0000, v133
	v_pk_fma_f32 v[24:25], v[24:25], v[150:151], v[76:77]
	v_lshlrev_b32_e32 v74, 16, v134
	v_and_b32_e32 v75, 0xffff0000, v134
	v_pk_fma_f32 v[18:19], v[18:19], v[152:153], v[74:75]
	v_lshlrev_b32_e32 v76, 16, v135
	v_and_b32_e32 v77, 0xffff0000, v135
	v_pk_fma_f32 v[20:21], v[20:21], v[154:155], v[76:77]
	v_cvt_pk_bf16_f32 v22, v22, v23
	v_cvt_pk_bf16_f32 v23, v24, v25
	v_cvt_pk_bf16_f32 v24, v18, v19
	v_cvt_pk_bf16_f32 v25, v20, v21
	v_add_u32_e32 v81, 0x50000, v79
	global_store_dwordx4 v81, v[22:25], s[28:29] offset:256
	s_waitcnt vmcnt(12)
	v_lshlrev_b32_e32 v74, 16, v188
	v_and_b32_e32 v75, 0xffff0000, v188
	v_pk_fma_f32 v[14:15], v[14:15], v[82:83], v[74:75]
	v_lshlrev_b32_e32 v76, 16, v189
	v_and_b32_e32 v77, 0xffff0000, v189
	v_pk_fma_f32 v[16:17], v[16:17], v[84:85], v[76:77]
	v_lshlrev_b32_e32 v74, 16, v190
	v_and_b32_e32 v75, 0xffff0000, v190
	v_pk_fma_f32 v[10:11], v[10:11], v[90:91], v[74:75]
	v_lshlrev_b32_e32 v76, 16, v191
	v_and_b32_e32 v77, 0xffff0000, v191
	v_pk_fma_f32 v[12:13], v[12:13], v[92:93], v[76:77]
	v_cvt_pk_bf16_f32 v14, v14, v15
	v_cvt_pk_bf16_f32 v15, v16, v17
	v_cvt_pk_bf16_f32 v16, v10, v11
	v_cvt_pk_bf16_f32 v17, v12, v13
	v_add_u32_e32 v81, 0x58000, v79
	global_store_dwordx4 v81, v[14:17], s[28:29]
	s_waitcnt vmcnt(12)
	v_lshlrev_b32_e32 v74, 16, v124
	v_and_b32_e32 v75, 0xffff0000, v124
	v_pk_fma_f32 v[6:7], v[6:7], v[148:149], v[74:75]
	v_lshlrev_b32_e32 v76, 16, v125
	v_and_b32_e32 v77, 0xffff0000, v125
	v_pk_fma_f32 v[8:9], v[8:9], v[150:151], v[76:77]
	v_lshlrev_b32_e32 v74, 16, v126
	v_and_b32_e32 v75, 0xffff0000, v126
	v_pk_fma_f32 v[2:3], v[2:3], v[152:153], v[74:75]
	v_lshlrev_b32_e32 v76, 16, v127
	v_and_b32_e32 v77, 0xffff0000, v127
	v_pk_fma_f32 v[4:5], v[4:5], v[154:155], v[76:77]
	v_cvt_pk_bf16_f32 v6, v6, v7
	v_cvt_pk_bf16_f32 v7, v8, v9
	v_cvt_pk_bf16_f32 v8, v2, v3
	v_cvt_pk_bf16_f32 v9, v4, v5
	v_add_u32_e32 v81, 0x58000, v79
	global_store_dwordx4 v81, v[6:9], s[28:29] offset:256
	s_nop 1
.Lresid_out_done:
	s_mov_b64 s[28:29], 0x2c000
	s_andn2_b64 vcc, exec, s[4:5]
	s_mov_b64 s[4:5], -1
	s_cbranch_vccnz .LBB13_918
	s_andn2_b64 vcc, exec, s[12:13]
	s_cbranch_vccnz .LBB13_917
	s_barrier
	s_branch .LBB13_917

; __device__ __forceinline__ unsigned pk2(float lo, float hi) { f32x2 v = {lo, hi}; return __builtin_bit_cast(unsigned, __builtin_convertvector(v, bf2_t)); }
; __device__ __forceinline__ float bflo(unsigned u) { return __uint_as_float(u << 16); }
; __device__ __forceinline__ float bfhi(unsigned u) { return __uint_as_float(u & 0xffff0000u); }
;     __device__ __forceinline__ void operator()(const f32x4 (&acc)[2][2][4][2], const Unit& u, int wr, int wc, int fr, int fq) const {
;         const int row0 = u.pm * BM + wr * 64 + fr, col0 = u.pn * BM + wc * 32 + 8 * fq;
;         const float* gv = gate + (size_t)(u.pm < 32 ? 0 : (u.pm < 64 ? 1 : 2)) * 6 * D;
;         f32x4 g4[2][2];
; #pragma unroll
;         for (int bj = 0; bj < 2; ++bj)
; #pragma unroll
;             for (int n = 0; n < 2; ++n) g4[bj][n] = *(const f32x4*)(gv + col0 + bj * HALF + 4 * n);
; #pragma unroll
;         for (int ai = 0; ai < 2; ++ai)
; #pragma unroll
;             for (int m = 0; m < 4; ++m) { const size_t ro = (size_t)(row0 + ai * HALF + m * 16) * D + col0;
; #pragma unroll
;                 for (int bj = 0; bj < 2; ++bj) { const size_t off = ro + bj * HALF;
;                     f32x4 b0, b1;
;                     if (base32) { b0 = *(const f32x4*)(base32 + off); b1 = *(const f32x4*)(base32 + off + 4); }
;                     else { const u32x4 hb = *(const u32x4*)(base + off); b0 = (f32x4){bflo(hb.x), bfhi(hb.x), bflo(hb.y), bfhi(hb.y)}; b1 = (f32x4){bflo(hb.z), bfhi(hb.z), bflo(hb.w), bfhi(hb.w)}; }
;                     const f32x4 o0 = b0 + g4[bj][0] * acc[ai][bj][m][0], o1 = b1 + g4[bj][1] * acc[ai][bj][m][1];
;                     u32x4 w; w.x = pk2(o0[0], o0[1]); w.y = pk2(o0[2], o0[3]); w.z = pk2(o1[0], o1[1]); w.w = pk2(o1[2], o1[3]);
;                     st16w(H + off, w); } }
;     }
; __global__ void __launch_bounds__(NWAVES * 64, 2) mk_fwd(Args args) {
;     ...
;                 const bf16* WD = (const bf16*)(ws + WS_FF + (l >> 1) * FF_STRIDE) + (size_t)2 * DFF * D; const float* g2 = (const float*)(ws + WS_MOD) + (size_t)l * 18 * D + 5 * D;
;                 pg8::Gemm g{(const bf16*)(ws + WS_HID), WD, ML, D, DFF}; pg8::StaticOrder S; S.init(ML, D, F.G, F.bx, DOWN_LIFO ? 2 : 0);
;                 pg8::EpiResid E{(bf16*)(ws + WS_H), g2, (const bf16*)(ws + WS_H), nullptr};
;                 pg8::gemm_phase<pg8::EpiResid, pg8::StaticOrder, true, true>(ring, g, S, E);
.LBB13_1541:
	s_cmp_lt_i32 s52, 64
	s_movk_i32 s16, 0x1800
	s_cselect_b32 s16, s16, 0x3000
	s_cmp_gt_i32 s52, 31
	s_cselect_b32 s16, s16, 0
	s_lshl_b32 s16, s16, 2
	s_add_u32 s16, s46, s16
	s_addc_u32 s17, s47, 0
	v_lshl_add_u32 v52, s52, 8, v166
	v_lshl_or_b32 v53, s60, 8, v168
	v_lshlrev_b32_e32 v50, 2, v53
	global_load_dwordx4 v[62:65], v50, s[16:17] offset:16
	global_load_dwordx4 v[58:61], v50, s[16:17]
	global_load_dwordx4 v[170:173], v50, s[16:17] offset:528
	global_load_dwordx4 v[160:163], v50, s[16:17] offset:512
	v_lshlrev_b32_e32 v51, 11, v52
	v_lshl_add_u32 v51, v53, 1, v51
	global_load_dwordx4 v[174:177], v51, s[8:9]
	global_load_dwordx4 v[178:181], v51, s[8:9] offset:256
	v_add_u32_e32 v52, 0x8000, v51
	global_load_dwordx4 v[182:185], v52, s[8:9]
	v_add_u32_e32 v52, 0x8000, v51
	global_load_dwordx4 v[186:189], v52, s[8:9] offset:256
	v_add_u32_e32 v52, 0x10000, v51
	global_load_dwordx4 v[190:193], v52, s[8:9]
	v_add_u32_e32 v52, 0x10000, v51
	global_load_dwordx4 v[194:197], v52, s[8:9] offset:256
	v_add_u32_e32 v52, 0x18000, v51
	global_load_dwordx4 v[208:211], v52, s[8:9]
	v_add_u32_e32 v52, 0x18000, v51
	global_load_dwordx4 v[212:215], v52, s[8:9] offset:256
	v_add_u32_e32 v52, 0x40000, v51
	global_load_dwordx4 v[216:219], v52, s[8:9]
	v_add_u32_e32 v52, 0x40000, v51
	global_load_dwordx4 v[220:223], v52, s[8:9] offset:256
	s_waitcnt vmcnt(9)
	v_lshlrev_b32_e32 v42, 16, v174
	v_and_b32_e32 v43, 0xffff0000, v174
	v_pk_fma_f32 v[144:145], v[144:145], v[58:59], v[42:43]
	v_lshlrev_b32_e32 v44, 16, v175
	v_and_b32_e32 v45, 0xffff0000, v175
	v_pk_fma_f32 v[146:147], v[146:147], v[60:61], v[44:45]
	v_lshlrev_b32_e32 v42, 16, v176
	v_and_b32_e32 v43, 0xffff0000, v176
	v_pk_fma_f32 v[140:141], v[140:141], v[62:63], v[42:43]
	v_lshlrev_b32_e32 v44, 16, v177
	v_and_b32_e32 v45, 0xffff0000, v177
	v_pk_fma_f32 v[142:143], v[142:143], v[64:65], v[44:45]
	v_cvt_pk_bf16_f32 v144, v144, v145
	v_cvt_pk_bf16_f32 v145, v146, v147
	v_cvt_pk_bf16_f32 v146, v140, v141
	v_cvt_pk_bf16_f32 v147, v142, v143
	global_store_dwordx4 v51, v[144:147], s[8:9]
	v_add_u32_e32 v52, 0x48000, v51
	global_load_dwordx4 v[174:177], v52, s[8:9]
	v_add_u32_e32 v52, 0x48000, v51
	global_load_dwordx4 v[140:143], v52, s[8:9] offset:256
	s_waitcnt vmcnt(11)
	v_lshlrev_b32_e32 v42, 16, v178
	v_and_b32_e32 v43, 0xffff0000, v178
	v_pk_fma_f32 v[136:137], v[136:137], v[160:161], v[42:43]
	v_lshlrev_b32_e32 v44, 16, v179
	v_and_b32_e32 v45, 0xffff0000, v179
	v_pk_fma_f32 v[138:139], v[138:139], v[162:163], v[44:45]
	v_lshlrev_b32_e32 v42, 16, v180
	v_and_b32_e32 v43, 0xffff0000, v180
	v_pk_fma_f32 v[132:133], v[132:133], v[170:171], v[42:43]
	v_lshlrev_b32_e32 v44, 16, v181
	v_and_b32_e32 v45, 0xffff0000, v181
	v_pk_fma_f32 v[134:135], v[134:135], v[172:173], v[44:45]
	v_cvt_pk_bf16_f32 v136, v136, v137
	v_cvt_pk_bf16_f32 v137, v138, v139
	v_cvt_pk_bf16_f32 v138, v132, v133
	v_cvt_pk_bf16_f32 v139, v134, v135
	global_store_dwordx4 v51, v[136:139], s[8:9] offset:256
	v_add_u32_e32 v52, 0x50000, v51
	global_load_dwordx4 v[178:181], v52, s[8:9]
	v_add_u32_e32 v52, 0x50000, v51
	global_load_dwordx4 v[132:135], v52, s[8:9] offset:256
	s_waitcnt vmcnt(13)
	v_lshlrev_b32_e32 v42, 16, v182
	v_and_b32_e32 v43, 0xffff0000, v182
	v_pk_fma_f32 v[128:129], v[128:129], v[58:59], v[42:43]
	v_lshlrev_b32_e32 v44, 16, v183
	v_and_b32_e32 v45, 0xffff0000, v183
	v_pk_fma_f32 v[130:131], v[130:131], v[60:61], v[44:45]
	v_lshlrev_b32_e32 v42, 16, v184
	v_and_b32_e32 v43, 0xffff0000, v184
	v_pk_fma_f32 v[124:125], v[124:125], v[62:63], v[42:43]
	v_lshlrev_b32_e32 v44, 16, v185
	v_and_b32_e32 v45, 0xffff0000, v185
	v_pk_fma_f32 v[126:127], v[126:127], v[64:65], v[44:45]
	v_cvt_pk_bf16_f32 v128, v128, v129
	v_cvt_pk_bf16_f32 v129, v130, v131
	v_cvt_pk_bf16_f32 v130, v124, v125
	v_cvt_pk_bf16_f32 v131, v126, v127
	v_add_u32_e32 v53, 0x8000, v51
	global_store_dwordx4 v53, v[128:131], s[8:9]
	v_add_u32_e32 v52, 0x58000, v51
	global_load_dwordx4 v[182:185], v52, s[8:9]
	v_add_u32_e32 v52, 0x58000, v51
	global_load_dwordx4 v[124:127], v52, s[8:9] offset:256
	s_waitcnt vmcnt(15)
	v_lshlrev_b32_e32 v42, 16, v186
	v_and_b32_e32 v43, 0xffff0000, v186
	v_pk_fma_f32 v[120:121], v[120:121], v[160:161], v[42:43]
	v_lshlrev_b32_e32 v44, 16, v187
	v_and_b32_e32 v45, 0xffff0000, v187
	v_pk_fma_f32 v[122:123], v[122:123], v[162:163], v[44:45]
	v_lshlrev_b32_e32 v42, 16, v188
	v_and_b32_e32 v43, 0xffff0000, v188
	v_pk_fma_f32 v[116:117], v[116:117], v[170:171], v[42:43]
	v_lshlrev_b32_e32 v44, 16, v189
	v_and_b32_e32 v45, 0xffff0000, v189
	v_pk_fma_f32 v[118:119], v[118:119], v[172:173], v[44:45]
	v_cvt_pk_bf16_f32 v120, v120, v121
	v_cvt_pk_bf16_f32 v121, v122, v123
	v_cvt_pk_bf16_f32 v122, v116, v117
	v_cvt_pk_bf16_f32 v123, v118, v119
	v_add_u32_e32 v53, 0x8000, v51
	global_store_dwordx4 v53, v[120:123], s[8:9] offset:256
	s_waitcnt vmcnt(15)
	v_lshlrev_b32_e32 v42, 16, v190
	v_and_b32_e32 v43, 0xffff0000, v190
	v_pk_fma_f32 v[112:113], v[112:113], v[58:59], v[42:43]
	v_lshlrev_b32_e32 v44, 16, v191
	v_and_b32_e32 v45, 0xffff0000, v191
	v_pk_fma_f32 v[114:115], v[114:115], v[60:61], v[44:45]
	v_lshlrev_b32_e32 v42, 16, v192
	v_and_b32_e32 v43, 0xffff0000, v192
	v_pk_fma_f32 v[108:109], v[108:109], v[62:63], v[42:43]
	v_lshlrev_b32_e32 v44, 16, v193
	v_and_b32_e32 v45, 0xffff0000, v193
	v_pk_fma_f32 v[110:111], v[110:111], v[64:65], v[44:45]
	v_cvt_pk_bf16_f32 v112, v112, v113
	v_cvt_pk_bf16_f32 v113, v114, v115
	v_cvt_pk_bf16_f32 v114, v108, v109
	v_cvt_pk_bf16_f32 v115, v110, v111
	v_add_u32_e32 v53, 0x10000, v51
	global_store_dwordx4 v53, v[112:115], s[8:9]
	s_waitcnt vmcnt(15)
; __device__ __forceinline__ unsigned pk2(float lo, float hi) { f32x2 v = {lo, hi}; return __builtin_bit_cast(unsigned, __builtin_convertvector(v, bf2_t)); }
; template <int BIT = 0> __device__ __forceinline__ void st16w(void* p, u32x4 v) { if ((WT_STORES >> BIT) & 1) asm volatile("global_store_dwordx4 %0, %1, off sc1\n\ts_nop 1" :: "v"(p), "v"(v) : "memory"); else *(u32x4*)p = v; }
; __device__ __forceinline__ float bflo(unsigned u) { return __uint_as_float(u << 16); }
; __device__ __forceinline__ float bfhi(unsigned u) { return __uint_as_float(u & 0xffff0000u); }
;     __device__ __forceinline__ void operator()(const f32x4 (&acc)[2][2][4][2], const Unit& u, int wr, int wc, int fr, int fq) const {
;     ...
;         for (int ai = 0; ai < 2; ++ai)
; #pragma unroll
;             for (int m = 0; m < 4; ++m) { const size_t ro = (size_t)(row0 + ai * HALF + m * 16) * D + col0;
; #pragma unroll
;                 for (int bj = 0; bj < 2; ++bj) { const size_t off = ro + bj * HALF;
;                     f32x4 b0, b1;
;                     if (base32) { b0 = *(const f32x4*)(base32 + off); b1 = *(const f32x4*)(base32 + off + 4); }
;                     else { const u32x4 hb = *(const u32x4*)(base + off); b0 = (f32x4){bflo(hb.x), bfhi(hb.x), bflo(hb.y), bfhi(hb.y)}; b1 = (f32x4){bflo(hb.z), bfhi(hb.z), bflo(hb.w), bfhi(hb.w)}; }
;                     const f32x4 o0 = b0 + g4[bj][0] * acc[ai][bj][m][0], o1 = b1 + g4[bj][1] * acc[ai][bj][m][1];
;                     u32x4 w; w.x = pk2(o0[0], o0[1]); w.y = pk2(o0[2], o0[3]); w.z = pk2(o1[0], o1[1]); w.w = pk2(o1[2], o1[3]);
;                     st16w(H + off, w); } }
	v_lshlrev_b32_e32 v42, 16, v194
	v_and_b32_e32 v43, 0xffff0000, v194
	v_pk_fma_f32 v[104:105], v[104:105], v[160:161], v[42:43]
	v_lshlrev_b32_e32 v44, 16, v195
	v_and_b32_e32 v45, 0xffff0000, v195
	v_pk_fma_f32 v[106:107], v[106:107], v[162:163], v[44:45]
	v_lshlrev_b32_e32 v42, 16, v196
	v_and_b32_e32 v43, 0xffff0000, v196
	v_pk_fma_f32 v[100:101], v[100:101], v[170:171], v[42:43]
	v_lshlrev_b32_e32 v44, 16, v197
	v_and_b32_e32 v45, 0xffff0000, v197
	v_pk_fma_f32 v[102:103], v[102:103], v[172:173], v[44:45]
	v_cvt_pk_bf16_f32 v104, v104, v105
	v_cvt_pk_bf16_f32 v105, v106, v107
	v_cvt_pk_bf16_f32 v106, v100, v101
	v_cvt_pk_bf16_f32 v107, v102, v103
	v_add_u32_e32 v53, 0x10000, v51
	global_store_dwordx4 v53, v[104:107], s[8:9] offset:256
	s_waitcnt vmcnt(15)
	v_lshlrev_b32_e32 v42, 16, v208
	v_and_b32_e32 v43, 0xffff0000, v208
	v_pk_fma_f32 v[94:95], v[94:95], v[58:59], v[42:43]
	v_lshlrev_b32_e32 v44, 16, v209
	v_and_b32_e32 v45, 0xffff0000, v209
	v_pk_fma_f32 v[96:97], v[96:97], v[60:61], v[44:45]
	v_lshlrev_b32_e32 v42, 16, v210
	v_and_b32_e32 v43, 0xffff0000, v210
	v_pk_fma_f32 v[90:91], v[90:91], v[62:63], v[42:43]
	v_lshlrev_b32_e32 v44, 16, v211
	v_and_b32_e32 v45, 0xffff0000, v211
	v_pk_fma_f32 v[92:93], v[92:93], v[64:65], v[44:45]
	v_cvt_pk_bf16_f32 v94, v94, v95
	v_cvt_pk_bf16_f32 v95, v96, v97
	v_cvt_pk_bf16_f32 v96, v90, v91
	v_cvt_pk_bf16_f32 v97, v92, v93
	v_add_u32_e32 v53, 0x18000, v51
	global_store_dwordx4 v53, v[94:97], s[8:9]
	s_waitcnt vmcnt(15)
	v_lshlrev_b32_e32 v42, 16, v212
	v_and_b32_e32 v43, 0xffff0000, v212
	v_pk_fma_f32 v[86:87], v[86:87], v[160:161], v[42:43]
	v_lshlrev_b32_e32 v44, 16, v213
	v_and_b32_e32 v45, 0xffff0000, v213
	v_pk_fma_f32 v[88:89], v[88:89], v[162:163], v[44:45]
	v_lshlrev_b32_e32 v42, 16, v214
	v_and_b32_e32 v43, 0xffff0000, v214
	v_pk_fma_f32 v[82:83], v[82:83], v[170:171], v[42:43]
	v_lshlrev_b32_e32 v44, 16, v215
	v_and_b32_e32 v45, 0xffff0000, v215
	v_pk_fma_f32 v[84:85], v[84:85], v[172:173], v[44:45]
	v_cvt_pk_bf16_f32 v86, v86, v87
	v_cvt_pk_bf16_f32 v87, v88, v89
	v_cvt_pk_bf16_f32 v88, v82, v83
	v_cvt_pk_bf16_f32 v89, v84, v85
	v_add_u32_e32 v53, 0x18000, v51
	global_store_dwordx4 v53, v[86:89], s[8:9] offset:256
	s_waitcnt vmcnt(15)
	v_lshlrev_b32_e32 v42, 16, v216
	v_and_b32_e32 v43, 0xffff0000, v216
	v_pk_fma_f32 v[78:79], v[78:79], v[58:59], v[42:43]
	v_lshlrev_b32_e32 v44, 16, v217
	v_and_b32_e32 v45, 0xffff0000, v217
	v_pk_fma_f32 v[80:81], v[80:81], v[60:61], v[44:45]
	v_lshlrev_b32_e32 v42, 16, v218
	v_and_b32_e32 v43, 0xffff0000, v218
	v_pk_fma_f32 v[74:75], v[74:75], v[62:63], v[42:43]
	v_lshlrev_b32_e32 v44, 16, v219
	v_and_b32_e32 v45, 0xffff0000, v219
	v_pk_fma_f32 v[76:77], v[76:77], v[64:65], v[44:45]
	v_cvt_pk_bf16_f32 v78, v78, v79
	v_cvt_pk_bf16_f32 v79, v80, v81
	v_cvt_pk_bf16_f32 v80, v74, v75
	v_cvt_pk_bf16_f32 v81, v76, v77
	v_add_u32_e32 v53, 0x40000, v51
	global_store_dwordx4 v53, v[78:81], s[8:9]
	s_waitcnt vmcnt(15)
	v_lshlrev_b32_e32 v42, 16, v220
	v_and_b32_e32 v43, 0xffff0000, v220
	v_pk_fma_f32 v[70:71], v[70:71], v[160:161], v[42:43]
	v_lshlrev_b32_e32 v44, 16, v221
	v_and_b32_e32 v45, 0xffff0000, v221
	v_pk_fma_f32 v[72:73], v[72:73], v[162:163], v[44:45]
	v_lshlrev_b32_e32 v42, 16, v222
	v_and_b32_e32 v43, 0xffff0000, v222
	v_pk_fma_f32 v[66:67], v[66:67], v[170:171], v[42:43]
	v_lshlrev_b32_e32 v44, 16, v223
	v_and_b32_e32 v45, 0xffff0000, v223
	v_pk_fma_f32 v[68:69], v[68:69], v[172:173], v[44:45]
	v_cvt_pk_bf16_f32 v70, v70, v71
	v_cvt_pk_bf16_f32 v71, v72, v73
	v_cvt_pk_bf16_f32 v72, v66, v67
	v_cvt_pk_bf16_f32 v73, v68, v69
	v_add_u32_e32 v53, 0x40000, v51
	global_store_dwordx4 v53, v[70:73], s[8:9] offset:256
	s_waitcnt vmcnt(14)
	v_lshlrev_b32_e32 v42, 16, v174
	v_and_b32_e32 v43, 0xffff0000, v174
	v_pk_fma_f32 v[54:55], v[54:55], v[58:59], v[42:43]
	v_lshlrev_b32_e32 v44, 16, v175
	v_and_b32_e32 v45, 0xffff0000, v175
	v_pk_fma_f32 v[56:57], v[56:57], v[60:61], v[44:45]
	v_lshlrev_b32_e32 v42, 16, v176
	v_and_b32_e32 v43, 0xffff0000, v176
	v_pk_fma_f32 v[46:47], v[46:47], v[62:63], v[42:43]
	v_lshlrev_b32_e32 v44, 16, v177
	v_and_b32_e32 v45, 0xffff0000, v177
	v_pk_fma_f32 v[48:49], v[48:49], v[64:65], v[44:45]
	v_cvt_pk_bf16_f32 v54, v54, v55
	v_cvt_pk_bf16_f32 v55, v56, v57
	v_cvt_pk_bf16_f32 v56, v46, v47
	v_cvt_pk_bf16_f32 v57, v48, v49
	v_add_u32_e32 v53, 0x48000, v51
	global_store_dwordx4 v53, v[54:57], s[8:9]
	s_waitcnt vmcnt(14)
; __device__ __forceinline__ unsigned pk2(float lo, float hi) { f32x2 v = {lo, hi}; return __builtin_bit_cast(unsigned, __builtin_convertvector(v, bf2_t)); }
; template <int BIT = 0> __device__ __forceinline__ void st16w(void* p, u32x4 v) { if ((WT_STORES >> BIT) & 1) asm volatile("global_store_dwordx4 %0, %1, off sc1\n\ts_nop 1" :: "v"(p), "v"(v) : "memory"); else *(u32x4*)p = v; }
; __device__ __forceinline__ float bflo(unsigned u) { return __uint_as_float(u << 16); }
; __device__ __forceinline__ float bfhi(unsigned u) { return __uint_as_float(u & 0xffff0000u); }
;     __device__ __forceinline__ void operator()(const f32x4 (&acc)[2][2][4][2], const Unit& u, int wr, int wc, int fr, int fq) const {
;     ...
;         for (int ai = 0; ai < 2; ++ai)
; #pragma unroll
;             for (int m = 0; m < 4; ++m) { const size_t ro = (size_t)(row0 + ai * HALF + m * 16) * D + col0;
; #pragma unroll
;                 for (int bj = 0; bj < 2; ++bj) { const size_t off = ro + bj * HALF;
;                     f32x4 b0, b1;
;                     if (base32) { b0 = *(const f32x4*)(base32 + off); b1 = *(const f32x4*)(base32 + off + 4); }
;                     else { const u32x4 hb = *(const u32x4*)(base + off); b0 = (f32x4){bflo(hb.x), bfhi(hb.x), bflo(hb.y), bfhi(hb.y)}; b1 = (f32x4){bflo(hb.z), bfhi(hb.z), bflo(hb.w), bfhi(hb.w)}; }
;                     const f32x4 o0 = b0 + g4[bj][0] * acc[ai][bj][m][0], o1 = b1 + g4[bj][1] * acc[ai][bj][m][1];
;                     u32x4 w; w.x = pk2(o0[0], o0[1]); w.y = pk2(o0[2], o0[3]); w.z = pk2(o1[0], o1[1]); w.w = pk2(o1[2], o1[3]);
;                     st16w(H + off, w); } }
	v_lshlrev_b32_e32 v42, 16, v140
	v_and_b32_e32 v43, 0xffff0000, v140
	v_pk_fma_f32 v[38:39], v[38:39], v[160:161], v[42:43]
	v_lshlrev_b32_e32 v44, 16, v141
	v_and_b32_e32 v45, 0xffff0000, v141
	v_pk_fma_f32 v[40:41], v[40:41], v[162:163], v[44:45]
	v_lshlrev_b32_e32 v42, 16, v142
	v_and_b32_e32 v43, 0xffff0000, v142
	v_pk_fma_f32 v[34:35], v[34:35], v[170:171], v[42:43]
	v_lshlrev_b32_e32 v44, 16, v143
	v_and_b32_e32 v45, 0xffff0000, v143
	v_pk_fma_f32 v[36:37], v[36:37], v[172:173], v[44:45]
	v_cvt_pk_bf16_f32 v38, v38, v39
	v_cvt_pk_bf16_f32 v39, v40, v41
	v_cvt_pk_bf16_f32 v40, v34, v35
	v_cvt_pk_bf16_f32 v41, v36, v37
	v_add_u32_e32 v53, 0x48000, v51
	global_store_dwordx4 v53, v[38:41], s[8:9] offset:256
	s_waitcnt vmcnt(13)
	v_lshlrev_b32_e32 v42, 16, v178
	v_and_b32_e32 v43, 0xffff0000, v178
	v_pk_fma_f32 v[30:31], v[30:31], v[58:59], v[42:43]
	v_lshlrev_b32_e32 v44, 16, v179
	v_and_b32_e32 v45, 0xffff0000, v179
	v_pk_fma_f32 v[32:33], v[32:33], v[60:61], v[44:45]
	v_lshlrev_b32_e32 v42, 16, v180
	v_and_b32_e32 v43, 0xffff0000, v180
	v_pk_fma_f32 v[26:27], v[26:27], v[62:63], v[42:43]
	v_lshlrev_b32_e32 v44, 16, v181
	v_and_b32_e32 v45, 0xffff0000, v181
	v_pk_fma_f32 v[28:29], v[28:29], v[64:65], v[44:45]
	v_cvt_pk_bf16_f32 v30, v30, v31
	v_cvt_pk_bf16_f32 v31, v32, v33
	v_cvt_pk_bf16_f32 v32, v26, v27
	v_cvt_pk_bf16_f32 v33, v28, v29
	v_add_u32_e32 v53, 0x50000, v51
	global_store_dwordx4 v53, v[30:33], s[8:9]
	s_waitcnt vmcnt(13)
	v_lshlrev_b32_e32 v42, 16, v132
	v_and_b32_e32 v43, 0xffff0000, v132
	v_pk_fma_f32 v[22:23], v[22:23], v[160:161], v[42:43]
	v_lshlrev_b32_e32 v44, 16, v133
	v_and_b32_e32 v45, 0xffff0000, v133
	v_pk_fma_f32 v[24:25], v[24:25], v[162:163], v[44:45]
	v_lshlrev_b32_e32 v42, 16, v134
	v_and_b32_e32 v43, 0xffff0000, v134
	v_pk_fma_f32 v[18:19], v[18:19], v[170:171], v[42:43]
	v_lshlrev_b32_e32 v44, 16, v135
	v_and_b32_e32 v45, 0xffff0000, v135
	v_pk_fma_f32 v[20:21], v[20:21], v[172:173], v[44:45]
	v_cvt_pk_bf16_f32 v22, v22, v23
	v_cvt_pk_bf16_f32 v23, v24, v25
	v_cvt_pk_bf16_f32 v24, v18, v19
	v_cvt_pk_bf16_f32 v25, v20, v21
	v_add_u32_e32 v53, 0x50000, v51
	global_store_dwordx4 v53, v[22:25], s[8:9] offset:256
	s_waitcnt vmcnt(12)
	v_lshlrev_b32_e32 v42, 16, v182
	v_and_b32_e32 v43, 0xffff0000, v182
	v_pk_fma_f32 v[14:15], v[14:15], v[58:59], v[42:43]
	v_lshlrev_b32_e32 v44, 16, v183
	v_and_b32_e32 v45, 0xffff0000, v183
	v_pk_fma_f32 v[16:17], v[16:17], v[60:61], v[44:45]
	v_lshlrev_b32_e32 v42, 16, v184
	v_and_b32_e32 v43, 0xffff0000, v184
	v_pk_fma_f32 v[10:11], v[10:11], v[62:63], v[42:43]
	v_lshlrev_b32_e32 v44, 16, v185
	v_and_b32_e32 v45, 0xffff0000, v185
	v_pk_fma_f32 v[12:13], v[12:13], v[64:65], v[44:45]
	v_cvt_pk_bf16_f32 v14, v14, v15
	v_cvt_pk_bf16_f32 v15, v16, v17
	v_cvt_pk_bf16_f32 v16, v10, v11
	v_cvt_pk_bf16_f32 v17, v12, v13
	v_add_u32_e32 v53, 0x58000, v51
	global_store_dwordx4 v53, v[14:17], s[8:9]
	s_waitcnt vmcnt(12)
	v_lshlrev_b32_e32 v42, 16, v124
	v_and_b32_e32 v43, 0xffff0000, v124
	v_pk_fma_f32 v[6:7], v[6:7], v[160:161], v[42:43]
	v_lshlrev_b32_e32 v44, 16, v125
	v_and_b32_e32 v45, 0xffff0000, v125
	v_pk_fma_f32 v[8:9], v[8:9], v[162:163], v[44:45]
	v_lshlrev_b32_e32 v42, 16, v126
	v_and_b32_e32 v43, 0xffff0000, v126
	v_pk_fma_f32 v[2:3], v[2:3], v[170:171], v[42:43]
	v_lshlrev_b32_e32 v44, 16, v127
	v_and_b32_e32 v45, 0xffff0000, v127
	v_pk_fma_f32 v[4:5], v[4:5], v[172:173], v[44:45]
	v_cvt_pk_bf16_f32 v6, v6, v7
	v_cvt_pk_bf16_f32 v7, v8, v9
	v_cvt_pk_bf16_f32 v8, v2, v3
	v_cvt_pk_bf16_f32 v9, v4, v5
	v_add_u32_e32 v53, 0x58000, v51
	global_store_dwordx4 v53, v[6:9], s[8:9] offset:256
	s_nop 1
	s_mov_b32 s64, 0x18000
	s_mov_b64 s[16:17], -1
	s_and_b64 vcc, exec, s[4:5]
	s_cbranch_vccnz .LBB13_1526
	s_andn2_b64 vcc, exec, s[10:11]
	s_cbranch_vccnz .LBB13_1525
	s_barrier
	s_branch .LBB13_1525

; template <int NS  > __device__ __forceinline__ f32x4 ctx_tile(Frame& F, const bf16* A, const bf16* Bt, int r0, int c0) {
;     constexpr int K = NS * 256;
;     const int lane = F.lane, w = F.wave, l15 = lane & 15, g = lane >> 4;
;     const bf16* ap = A + (size_t)(r0 + l15) * K + w * (K / 8) + 8 * g;
;     const bf16* bp = Bt + (size_t)(c0 + l15) * K + w * (K / 8) + 8 * g;
;     f32x4 acc[4][2];
; #pragma unroll
;     for (int rt = 0; rt < 4; ++rt) { acc[rt][0] = (f32x4){0.f, 0.f, 0.f, 0.f}; acc[rt][1] = (f32x4){0.f, 0.f, 0.f, 0.f}; }
; #pragma unroll 4
;     for (int s = 0; s < NS; ++s) {
;         bf16x8 af[4], bf[2];
; #pragma unroll
;         for (int rt = 0; rt < 4; ++rt) af[rt] = *(const bf16x8*)(ap + (size_t)(16 * rt) * K + 32 * s);
;         bf[0] = *(const bf16x8*)(bp + 32 * s); bf[1] = *(const bf16x8*)(bp + (size_t)16 * K + 32 * s);
; #pragma unroll
;         for (int rt = 0; rt < 4; ++rt) { acc[rt][0] = __builtin_amdgcn_mfma_f32_16x16x32_bf16(bf[0], af[rt], acc[rt][0], 0, 0, 0); acc[rt][1] = __builtin_amdgcn_mfma_f32_16x16x32_bf16(bf[1], af[rt], acc[rt][1], 0, 0, 0); }
; __global__ void __launch_bounds__(NWAVES * 64, 2) mk_fwd(Args args) {
;     ...
;                 for (int tl = F.vcu; tl < (np - npm) * 128; tl += F.G) {
;                     const int pm = npm + (tl >> 7), r0 = 256 * pm + 64 * ((tl >> 5) & 3), c0 = 32 * (tl & 31);
;                     const int e = __builtin_amdgcn_readfirstlane(((const int*)(ws + WS_PANELE))[pm]);
;                     const f32x4 s = ctx_tile<14>(F, (const bf16*)(ws + WS_HID), (const bf16*)(ws + WS_EXP + (l >> 1) * EXP_STRIDE) + (size_t)NE * 2 * DFE * D + (size_t)e * D * DFE, r0, c0);
.LBB13_1582:
	s_ashr_i32 s4, s29, 7
	s_add_i32 s4, s4, s36
	s_lshl_b32 s6, s29, 6
	s_and_b32 s6, s6, 0xc0
	s_lshl_b32 s15, s29, 3
	s_and_b32 s15, s15, 0x3e0
	s_lshl_b32 s7, s4, 8
	s_ashr_i32 s5, s4, 31
	v_or_b32_e32 v2, s15, v62
	s_or_b32 s16, s7, s6
	s_lshl_b64 s[4:5], s[4:5], 2
	v_mul_u32_u24_e32 v2, 0xe00, v2
	s_add_u32 s4, s2, s4
	v_lshlrev_b32_e32 v10, 1, v2
	v_or_b32_e32 v2, s16, v62
	s_addc_u32 s5, s3, s5
	v_mad_i64_i32 v[30:31], s[6:7], v2, s86, v[58:59]
	global_load_dword v12, v98, s[4:5]
	s_mov_b32 s4, 0x38000
	v_add_co_u32_e32 v32, vcc, s90, v30
	v_add_co_u32_e64 v50, s[4:5], s4, v30
	s_nop 0
	v_addc_co_u32_e32 v33, vcc, 0, v31, vcc
	v_addc_co_u32_e64 v51, vcc, 0, v31, s[4:5]
	v_mov_b32_e32 v11, v98
	s_mov_b32 s6, 0x54000
	v_mov_b32_e32 v61, v98
	v_add_co_u32_e64 v54, s[6:7], s6, v30
	s_nop 1
	v_addc_co_u32_e64 v55, vcc, 0, v31, s[6:7]
	global_load_dwordx4 v[68:71], v[30:31], off
	global_load_dwordx4 v[72:75], v[32:33], off
	global_load_dwordx4 v[76:79], v[50:51], off
	global_load_dwordx4 v[80:83], v[54:55], off
	global_load_dwordx4 v[84:87], v[30:31], off offset:64
	global_load_dwordx4 v[88:91], v[32:33], off offset:64
	global_load_dwordx4 v[92:95], v[50:51], off offset:64
	global_load_dwordx4 v[100:103], v[54:55], off offset:64
	global_load_dwordx4 v[104:107], v[30:31], off offset:128
	global_load_dwordx4 v[108:111], v[32:33], off offset:128
	global_load_dwordx4 v[112:115], v[50:51], off offset:128
	global_load_dwordx4 v[116:119], v[54:55], off offset:128
	global_load_dwordx4 v[120:123], v[30:31], off offset:192
	global_load_dwordx4 v[124:127], v[32:33], off offset:192
	global_load_dwordx4 v[128:131], v[50:51], off offset:192
	global_load_dwordx4 v[132:135], v[54:55], off offset:192
	global_load_dwordx4 v[136:139], v[30:31], off offset:256
	global_load_dwordx4 v[140:143], v[32:33], off offset:256
	global_load_dwordx4 v[144:147], v[50:51], off offset:256
	global_load_dwordx4 v[148:151], v[54:55], off offset:256
	global_load_dwordx4 v[152:155], v[30:31], off offset:320
	global_load_dwordx4 v[156:159], v[32:33], off offset:320
	global_load_dwordx4 v[160:163], v[50:51], off offset:320
	global_load_dwordx4 v[164:167], v[54:55], off offset:320
	s_waitcnt vmcnt(24)
	v_readfirstlane_b32 s4, v12
	s_mul_hi_i32 s5, s4, 0x700000
	s_mul_i32 s4, s4, 0x700000
	s_add_u32 s4, s34, s4
	s_addc_u32 s5, s35, s5
	v_lshl_add_u64 v[10:11], s[4:5], 0, v[10:11]
	v_lshl_add_u64 v[10:11], s[8:9], 1, v[10:11]
	v_lshl_add_u64 v[52:53], v[10:11], 0, v[60:61]
	v_add_co_u32_e32 v56, vcc, s90, v52
	s_nop 1
	v_addc_co_u32_e32 v57, vcc, 0, v53, vcc
	global_load_dwordx4 v[168:171], v[52:53], off
	global_load_dwordx4 v[172:175], v[56:57], off
	global_load_dwordx4 v[176:179], v[52:53], off offset:64
	global_load_dwordx4 v[180:183], v[56:57], off offset:64
	global_load_dwordx4 v[184:187], v[52:53], off offset:128
	global_load_dwordx4 v[188:191], v[56:57], off offset:128
	global_load_dwordx4 v[192:195], v[52:53], off offset:192
	global_load_dwordx4 v[208:211], v[56:57], off offset:192
	global_load_dwordx4 v[212:215], v[52:53], off offset:256
	global_load_dwordx4 v[216:219], v[56:57], off offset:256
	global_load_dwordx4 v[220:223], v[52:53], off offset:320
	global_load_dwordx4 v[224:227], v[56:57], off offset:320
	s_waitcnt vmcnt(10)
	v_mfma_f32_16x16x32_bf16 v[4:7], v[168:171], v[68:71], 0
	v_mfma_f32_16x16x32_bf16 v[8:11], v[172:175], v[68:71], 0
	v_mfma_f32_16x16x32_bf16 v[12:15], v[168:171], v[72:75], 0
	v_mfma_f32_16x16x32_bf16 v[16:19], v[172:175], v[72:75], 0
	v_mfma_f32_16x16x32_bf16 v[20:23], v[168:171], v[76:79], 0
	v_mfma_f32_16x16x32_bf16 v[24:27], v[172:175], v[76:79], 0
	v_mfma_f32_16x16x32_bf16 v[44:47], v[168:171], v[80:83], 0
	v_mfma_f32_16x16x32_bf16 v[244:247], v[172:175], v[80:83], 0
	global_load_dwordx4 v[228:231], v[30:31], off offset:384
	global_load_dwordx4 v[68:71], v[32:33], off offset:384
	global_load_dwordx4 v[72:75], v[50:51], off offset:384
	global_load_dwordx4 v[76:79], v[54:55], off offset:384
	global_load_dwordx4 v[80:83], v[52:53], off offset:384
	global_load_dwordx4 v[168:171], v[56:57], off offset:384
	s_waitcnt vmcnt(14)
	v_mfma_f32_16x16x32_bf16 v[4:7], v[176:179], v[84:87], v[4:7]
	v_mfma_f32_16x16x32_bf16 v[8:11], v[180:183], v[84:87], v[8:11]
	v_mfma_f32_16x16x32_bf16 v[12:15], v[176:179], v[88:91], v[12:15]
	v_mfma_f32_16x16x32_bf16 v[16:19], v[180:183], v[88:91], v[16:19]
	v_mfma_f32_16x16x32_bf16 v[20:23], v[176:179], v[92:95], v[20:23]
	v_mfma_f32_16x16x32_bf16 v[24:27], v[180:183], v[92:95], v[24:27]
	v_mfma_f32_16x16x32_bf16 v[44:47], v[176:179], v[100:103], v[44:47]
	v_mfma_f32_16x16x32_bf16 v[244:247], v[180:183], v[100:103], v[244:247]
	global_load_dwordx4 v[172:175], v[30:31], off offset:448
	global_load_dwordx4 v[84:87], v[32:33], off offset:448
	global_load_dwordx4 v[88:91], v[50:51], off offset:448
	global_load_dwordx4 v[92:95], v[54:55], off offset:448
	global_load_dwordx4 v[100:103], v[52:53], off offset:448
	global_load_dwordx4 v[176:179], v[56:57], off offset:448
	s_waitcnt vmcnt(18)
	v_mfma_f32_16x16x32_bf16 v[4:7], v[184:187], v[104:107], v[4:7]
	v_mfma_f32_16x16x32_bf16 v[8:11], v[188:191], v[104:107], v[8:11]
	v_mfma_f32_16x16x32_bf16 v[12:15], v[184:187], v[108:111], v[12:15]
	v_mfma_f32_16x16x32_bf16 v[16:19], v[188:191], v[108:111], v[16:19]
	v_mfma_f32_16x16x32_bf16 v[20:23], v[184:187], v[112:115], v[20:23]
	v_mfma_f32_16x16x32_bf16 v[24:27], v[188:191], v[112:115], v[24:27]
	v_mfma_f32_16x16x32_bf16 v[44:47], v[184:187], v[116:119], v[44:47]
	v_mfma_f32_16x16x32_bf16 v[244:247], v[188:191], v[116:119], v[244:247]
	global_load_dwordx4 v[180:183], v[30:31], off offset:512
	global_load_dwordx4 v[104:107], v[32:33], off offset:512
	global_load_dwordx4 v[108:111], v[50:51], off offset:512
	global_load_dwordx4 v[112:115], v[54:55], off offset:512
	global_load_dwordx4 v[116:119], v[52:53], off offset:512
	global_load_dwordx4 v[184:187], v[56:57], off offset:512
	s_waitcnt vmcnt(22)
; template <int NS  > __device__ __forceinline__ f32x4 ctx_tile(Frame& F, const bf16* A, const bf16* Bt, int r0, int c0) {
;     ...
; #pragma unroll 4
;     for (int s = 0; s < NS; ++s) {
;         bf16x8 af[4], bf[2];
; #pragma unroll
;         for (int rt = 0; rt < 4; ++rt) af[rt] = *(const bf16x8*)(ap + (size_t)(16 * rt) * K + 32 * s);
;         bf[0] = *(const bf16x8*)(bp + 32 * s); bf[1] = *(const bf16x8*)(bp + (size_t)16 * K + 32 * s);
; #pragma unroll
;         for (int rt = 0; rt < 4; ++rt) { acc[rt][0] = __builtin_amdgcn_mfma_f32_16x16x32_bf16(bf[0], af[rt], acc[rt][0], 0, 0, 0); acc[rt][1] = __builtin_amdgcn_mfma_f32_16x16x32_bf16(bf[1], af[rt], acc[rt][1], 0, 0, 0); }
;     }
	v_mfma_f32_16x16x32_bf16 v[4:7], v[192:195], v[120:123], v[4:7]
	v_mfma_f32_16x16x32_bf16 v[8:11], v[208:211], v[120:123], v[8:11]
	v_mfma_f32_16x16x32_bf16 v[12:15], v[192:195], v[124:127], v[12:15]
	v_mfma_f32_16x16x32_bf16 v[16:19], v[208:211], v[124:127], v[16:19]
	v_mfma_f32_16x16x32_bf16 v[20:23], v[192:195], v[128:131], v[20:23]
	v_mfma_f32_16x16x32_bf16 v[24:27], v[208:211], v[128:131], v[24:27]
	v_mfma_f32_16x16x32_bf16 v[44:47], v[192:195], v[132:135], v[44:47]
	v_mfma_f32_16x16x32_bf16 v[244:247], v[208:211], v[132:135], v[244:247]
	global_load_dwordx4 v[188:191], v[30:31], off offset:576
	global_load_dwordx4 v[120:123], v[32:33], off offset:576
	global_load_dwordx4 v[124:127], v[50:51], off offset:576
	global_load_dwordx4 v[128:131], v[54:55], off offset:576
	global_load_dwordx4 v[132:135], v[52:53], off offset:576
	global_load_dwordx4 v[192:195], v[56:57], off offset:576
	s_waitcnt vmcnt(26)
	v_mfma_f32_16x16x32_bf16 v[4:7], v[212:215], v[136:139], v[4:7]
	v_mfma_f32_16x16x32_bf16 v[8:11], v[216:219], v[136:139], v[8:11]
	v_mfma_f32_16x16x32_bf16 v[12:15], v[212:215], v[140:143], v[12:15]
	v_mfma_f32_16x16x32_bf16 v[16:19], v[216:219], v[140:143], v[16:19]
	v_mfma_f32_16x16x32_bf16 v[20:23], v[212:215], v[144:147], v[20:23]
	v_mfma_f32_16x16x32_bf16 v[24:27], v[216:219], v[144:147], v[24:27]
	v_mfma_f32_16x16x32_bf16 v[44:47], v[212:215], v[148:151], v[44:47]
	v_mfma_f32_16x16x32_bf16 v[244:247], v[216:219], v[148:151], v[244:247]
	global_load_dwordx4 v[208:211], v[30:31], off offset:640
	global_load_dwordx4 v[136:139], v[32:33], off offset:640
	global_load_dwordx4 v[140:143], v[50:51], off offset:640
	global_load_dwordx4 v[144:147], v[54:55], off offset:640
	global_load_dwordx4 v[148:151], v[52:53], off offset:640
	global_load_dwordx4 v[212:215], v[56:57], off offset:640
	s_waitcnt vmcnt(30)
	v_mfma_f32_16x16x32_bf16 v[4:7], v[220:223], v[152:155], v[4:7]
	v_mfma_f32_16x16x32_bf16 v[8:11], v[224:227], v[152:155], v[8:11]
	v_mfma_f32_16x16x32_bf16 v[12:15], v[220:223], v[156:159], v[12:15]
	v_mfma_f32_16x16x32_bf16 v[16:19], v[224:227], v[156:159], v[16:19]
	v_mfma_f32_16x16x32_bf16 v[20:23], v[220:223], v[160:163], v[20:23]
	v_mfma_f32_16x16x32_bf16 v[24:27], v[224:227], v[160:163], v[24:27]
	v_mfma_f32_16x16x32_bf16 v[44:47], v[220:223], v[164:167], v[44:47]
	v_mfma_f32_16x16x32_bf16 v[244:247], v[224:227], v[164:167], v[244:247]
	global_load_dwordx4 v[216:219], v[30:31], off offset:704
	global_load_dwordx4 v[152:155], v[32:33], off offset:704
	global_load_dwordx4 v[156:159], v[50:51], off offset:704
	global_load_dwordx4 v[160:163], v[54:55], off offset:704
	global_load_dwordx4 v[164:167], v[52:53], off offset:704
	global_load_dwordx4 v[220:223], v[56:57], off offset:704
	s_waitcnt vmcnt(30)
	v_mfma_f32_16x16x32_bf16 v[4:7], v[80:83], v[228:231], v[4:7]
	v_mfma_f32_16x16x32_bf16 v[8:11], v[168:171], v[228:231], v[8:11]
	v_mfma_f32_16x16x32_bf16 v[12:15], v[80:83], v[68:71], v[12:15]
	v_mfma_f32_16x16x32_bf16 v[16:19], v[168:171], v[68:71], v[16:19]
	v_mfma_f32_16x16x32_bf16 v[20:23], v[80:83], v[72:75], v[20:23]
	v_mfma_f32_16x16x32_bf16 v[24:27], v[168:171], v[72:75], v[24:27]
	v_mfma_f32_16x16x32_bf16 v[44:47], v[80:83], v[76:79], v[44:47]
	v_mfma_f32_16x16x32_bf16 v[244:247], v[168:171], v[76:79], v[244:247]
	global_load_dwordx4 v[224:227], v[30:31], off offset:768
	global_load_dwordx4 v[228:231], v[32:33], off offset:768
	global_load_dwordx4 v[68:71], v[50:51], off offset:768
	global_load_dwordx4 v[72:75], v[54:55], off offset:768
	global_load_dwordx4 v[76:79], v[52:53], off offset:768
	global_load_dwordx4 v[80:83], v[56:57], off offset:768
	s_waitcnt vmcnt(30)
	v_mfma_f32_16x16x32_bf16 v[4:7], v[100:103], v[172:175], v[4:7]
	v_mfma_f32_16x16x32_bf16 v[8:11], v[176:179], v[172:175], v[8:11]
	v_mfma_f32_16x16x32_bf16 v[12:15], v[100:103], v[84:87], v[12:15]
	v_mfma_f32_16x16x32_bf16 v[16:19], v[176:179], v[84:87], v[16:19]
	v_mfma_f32_16x16x32_bf16 v[20:23], v[100:103], v[88:91], v[20:23]
	v_mfma_f32_16x16x32_bf16 v[24:27], v[176:179], v[88:91], v[24:27]
	v_mfma_f32_16x16x32_bf16 v[44:47], v[100:103], v[92:95], v[44:47]
	v_mfma_f32_16x16x32_bf16 v[244:247], v[176:179], v[92:95], v[244:247]
	global_load_dwordx4 v[168:171], v[30:31], off offset:832
	global_load_dwordx4 v[172:175], v[32:33], off offset:832
	global_load_dwordx4 v[84:87], v[50:51], off offset:832
	global_load_dwordx4 v[88:91], v[54:55], off offset:832
	global_load_dwordx4 v[92:95], v[52:53], off offset:832
	global_load_dwordx4 v[100:103], v[56:57], off offset:832
	s_waitcnt vmcnt(30)
	v_mfma_f32_16x16x32_bf16 v[4:7], v[116:119], v[180:183], v[4:7]
	v_mfma_f32_16x16x32_bf16 v[8:11], v[184:187], v[180:183], v[8:11]
	v_mfma_f32_16x16x32_bf16 v[12:15], v[116:119], v[104:107], v[12:15]
	v_mfma_f32_16x16x32_bf16 v[16:19], v[184:187], v[104:107], v[16:19]
	v_mfma_f32_16x16x32_bf16 v[20:23], v[116:119], v[108:111], v[20:23]
	v_mfma_f32_16x16x32_bf16 v[24:27], v[184:187], v[108:111], v[24:27]
	v_mfma_f32_16x16x32_bf16 v[44:47], v[116:119], v[112:115], v[44:47]
	v_mfma_f32_16x16x32_bf16 v[244:247], v[184:187], v[112:115], v[244:247]
	s_waitcnt vmcnt(24)
; #define LAS __attribute__((address_space(3)))
; __device__ __forceinline__ unsigned pk2(float lo, float hi) { f32x2 v = {lo, hi}; return __builtin_bit_cast(unsigned, __builtin_convertvector(v, bf2_t)); }
; template <int NS  > __device__ __forceinline__ f32x4 ctx_tile(Frame& F, const bf16* A, const bf16* Bt, int r0, int c0) {
;     ...
;     for (int s = 0; s < NS; ++s) {
;         bf16x8 af[4], bf[2];
; #pragma unroll
;         for (int rt = 0; rt < 4; ++rt) af[rt] = *(const bf16x8*)(ap + (size_t)(16 * rt) * K + 32 * s);
;         bf[0] = *(const bf16x8*)(bp + 32 * s); bf[1] = *(const bf16x8*)(bp + (size_t)16 * K + 32 * s);
; #pragma unroll
;         for (int rt = 0; rt < 4; ++rt) { acc[rt][0] = __builtin_amdgcn_mfma_f32_16x16x32_bf16(bf[0], af[rt], acc[rt][0], 0, 0, 0); acc[rt][1] = __builtin_amdgcn_mfma_f32_16x16x32_bf16(bf[1], af[rt], acc[rt][1], 0, 0, 0); }
;     }
;     LAS f32x4* red = (LAS f32x4*)F.lds;
;     __syncthreads();
; #pragma unroll
;     for (int rt = 0; rt < 4; ++rt) { red[(w * 8 + 2 * rt) * 64 + lane] = acc[rt][0]; red[(w * 8 + 2 * rt + 1) * 64 + lane] = acc[rt][1]; }
;     __syncthreads();
;     const int tt = F.tid >> 6;
;     f32x4 v = red[tt * 64 + lane];
; #pragma unroll
;     for (int ww = 1; ww < 8; ++ww) v = v + red[(ww * 8 + tt) * 64 + lane];
;     return v;
; __global__ void __launch_bounds__(NWAVES * 64, 2) mk_fwd(Args args) {
;     ...
;                 for (int tl = F.vcu; tl < (np - npm) * 128; tl += F.G) {
;                     const int pm = npm + (tl >> 7), r0 = 256 * pm + 64 * ((tl >> 5) & 3), c0 = 32 * (tl & 31);
;                     const int e = __builtin_amdgcn_readfirstlane(((const int*)(ws + WS_PANELE))[pm]);
;                     const f32x4 s = ctx_tile<14>(F, (const bf16*)(ws + WS_HID), (const bf16*)(ws + WS_EXP + (l >> 1) * EXP_STRIDE) + (size_t)NE * 2 * DFE * D + (size_t)e * D * DFE, r0, c0);
;                     const int tt = F.tid >> 6; const size_t row = (size_t)(r0 + 16 * (tt >> 1) + (F.lane & 15)); const int col = c0 + 16 * (tt & 1) + 4 * (F.lane >> 4);
;                     u32x2 o2; o2.x = pk2(s[0], s[1]); o2.y = pk2(s[2], s[3]);
;                     *(u32x2*)((bf16*)(ws + WS_FS) + row * D + col) = o2;
;                 }
	v_mfma_f32_16x16x32_bf16 v[4:7], v[132:135], v[188:191], v[4:7]
	v_mfma_f32_16x16x32_bf16 v[8:11], v[192:195], v[188:191], v[8:11]
	v_mfma_f32_16x16x32_bf16 v[12:15], v[132:135], v[120:123], v[12:15]
	v_mfma_f32_16x16x32_bf16 v[16:19], v[192:195], v[120:123], v[16:19]
	v_mfma_f32_16x16x32_bf16 v[20:23], v[132:135], v[124:127], v[20:23]
	v_mfma_f32_16x16x32_bf16 v[24:27], v[192:195], v[124:127], v[24:27]
	v_mfma_f32_16x16x32_bf16 v[44:47], v[132:135], v[128:131], v[44:47]
	v_mfma_f32_16x16x32_bf16 v[244:247], v[192:195], v[128:131], v[244:247]
	s_waitcnt vmcnt(18)
	v_mfma_f32_16x16x32_bf16 v[4:7], v[148:151], v[208:211], v[4:7]
	v_mfma_f32_16x16x32_bf16 v[8:11], v[212:215], v[208:211], v[8:11]
	v_mfma_f32_16x16x32_bf16 v[12:15], v[148:151], v[136:139], v[12:15]
	v_mfma_f32_16x16x32_bf16 v[16:19], v[212:215], v[136:139], v[16:19]
	v_mfma_f32_16x16x32_bf16 v[20:23], v[148:151], v[140:143], v[20:23]
	v_mfma_f32_16x16x32_bf16 v[24:27], v[212:215], v[140:143], v[24:27]
	v_mfma_f32_16x16x32_bf16 v[44:47], v[148:151], v[144:147], v[44:47]
	v_mfma_f32_16x16x32_bf16 v[244:247], v[212:215], v[144:147], v[244:247]
	s_waitcnt vmcnt(12)
	v_mfma_f32_16x16x32_bf16 v[4:7], v[164:167], v[216:219], v[4:7]
	v_mfma_f32_16x16x32_bf16 v[8:11], v[220:223], v[216:219], v[8:11]
	v_mfma_f32_16x16x32_bf16 v[12:15], v[164:167], v[152:155], v[12:15]
	v_mfma_f32_16x16x32_bf16 v[16:19], v[220:223], v[152:155], v[16:19]
	v_mfma_f32_16x16x32_bf16 v[20:23], v[164:167], v[156:159], v[20:23]
	v_mfma_f32_16x16x32_bf16 v[24:27], v[220:223], v[156:159], v[24:27]
	v_mfma_f32_16x16x32_bf16 v[44:47], v[164:167], v[160:163], v[44:47]
	v_mfma_f32_16x16x32_bf16 v[244:247], v[220:223], v[160:163], v[244:247]
	s_waitcnt vmcnt(6)
	v_mfma_f32_16x16x32_bf16 v[4:7], v[76:79], v[224:227], v[4:7]
	v_mfma_f32_16x16x32_bf16 v[8:11], v[80:83], v[224:227], v[8:11]
	v_mfma_f32_16x16x32_bf16 v[12:15], v[76:79], v[228:231], v[12:15]
	v_mfma_f32_16x16x32_bf16 v[16:19], v[80:83], v[228:231], v[16:19]
	v_mfma_f32_16x16x32_bf16 v[20:23], v[76:79], v[68:71], v[20:23]
	v_mfma_f32_16x16x32_bf16 v[24:27], v[80:83], v[68:71], v[24:27]
	v_mfma_f32_16x16x32_bf16 v[44:47], v[76:79], v[72:75], v[44:47]
	v_mfma_f32_16x16x32_bf16 v[244:247], v[80:83], v[72:75], v[244:247]
	s_waitcnt vmcnt(0)
	v_mfma_f32_16x16x32_bf16 v[4:7], v[92:95], v[168:171], v[4:7]
	v_mfma_f32_16x16x32_bf16 v[8:11], v[100:103], v[168:171], v[8:11]
	v_mfma_f32_16x16x32_bf16 v[12:15], v[92:95], v[172:175], v[12:15]
	v_mfma_f32_16x16x32_bf16 v[16:19], v[100:103], v[172:175], v[16:19]
	v_mfma_f32_16x16x32_bf16 v[20:23], v[92:95], v[84:87], v[20:23]
	v_mfma_f32_16x16x32_bf16 v[24:27], v[100:103], v[84:87], v[24:27]
	v_mfma_f32_16x16x32_bf16 v[44:47], v[92:95], v[88:91], v[44:47]
	v_mfma_f32_16x16x32_bf16 v[244:247], v[100:103], v[88:91], v[244:247]
	v_or_b32_e32 v61, s15, v1
	s_add_i32 s29, s29, s28
	s_add_i32 s11, s11, s12
	s_add_i32 s13, s13, s14
	s_cmp_ge_i32 s29, s10
	v_mov_b32_e32 v67, v98
	s_barrier
	v_lshlrev_b32_e32 v66, 1, v61
	v_add_u32_e32 v42, s16, v65
	v_ashrrev_i32_e32 v43, 31, v42
	v_lshlrev_b64 v[42:43], 11, v[42:43]
	v_lshl_add_u64 v[38:39], s[0:1], 0, v[42:43]
	v_lshl_add_u64 v[38:39], v[38:39], 0, v[66:67]
	s_nop 7
	ds_write_b128 v63, v[4:7]
	ds_write_b128 v63, v[8:11] offset:1024
	ds_write_b128 v63, v[12:15] offset:2048
	ds_write_b128 v63, v[16:19] offset:3072
	ds_write_b128 v63, v[20:23] offset:4096
	ds_write_b128 v63, v[24:27] offset:5120
	ds_write_b128 v63, v[44:47] offset:6144
	ds_write_b128 v63, v[244:247] offset:7168
	s_waitcnt lgkmcnt(0)
	s_barrier
	ds_read_b128 v[2:5], v64
	ds_read_b128 v[6:9], v64 offset:8192
	ds_read_b128 v[10:13], v64 offset:16384
	ds_read_b128 v[14:17], v64 offset:24576
	ds_read_b128 v[18:21], v64 offset:32768
	ds_read_b128 v[22:25], v64 offset:40960
	ds_read_b128 v[26:29], v64 offset:49152
	ds_read_b128 v[30:33], v64 offset:57344
	s_waitcnt lgkmcnt(6)
	v_pk_add_f32 v[4:5], v[4:5], v[8:9]
	v_pk_add_f32 v[2:3], v[2:3], v[6:7]
	s_waitcnt lgkmcnt(5)
	v_pk_add_f32 v[4:5], v[4:5], v[12:13]
	v_pk_add_f32 v[2:3], v[2:3], v[10:11]
	s_waitcnt lgkmcnt(4)
	v_pk_add_f32 v[4:5], v[4:5], v[16:17]
	v_pk_add_f32 v[2:3], v[2:3], v[14:15]
	s_waitcnt lgkmcnt(3)
	v_pk_add_f32 v[4:5], v[4:5], v[20:21]
	v_pk_add_f32 v[2:3], v[2:3], v[18:19]
	s_waitcnt lgkmcnt(2)
	v_pk_add_f32 v[4:5], v[4:5], v[24:25]
	v_pk_add_f32 v[2:3], v[2:3], v[22:23]
	s_waitcnt lgkmcnt(1)
	v_pk_add_f32 v[4:5], v[4:5], v[28:29]
	v_pk_add_f32 v[2:3], v[2:3], v[26:27]
	s_waitcnt lgkmcnt(0)
	v_pk_add_f32 v[4:5], v[4:5], v[32:33]
	v_pk_add_f32 v[2:3], v[2:3], v[30:31]
	s_nop 0
	v_cvt_pk_bf16_f32 v2, v2, v3
	v_cvt_pk_bf16_f32 v3, v4, v5
	global_store_dwordx2 v[38:39], v[2:3], off
	s_cbranch_scc0 .LBB13_1582
